# router/placement/combine/QKV/scan phases: all stores write-through (sc1) and no L2 write-back at their seams (8 seams); combine rewrite; final RMSNorm rewrite
# baseline (speedup 1.0000x reference)
.LBB0_577:
	s_lshl_b32 s23, s28, 8
	s_ashr_i32 s28, s21, 2
	s_andn2_b32 s28, s28, 63
	v_and_b32_e32 v104, 63, v82
	s_add_i32 s28, s28, s23
	v_or_b32_e32 v66, s28, v104
	v_ashrrev_i32_e32 v67, 31, v66
	v_lshl_add_u64 v[66:67], v[66:67], 2, s[14:15]
	v_add_co_u32_e32 v68, vcc, s50, v66
	s_lshr_b32 s21, s21, 6
	s_nop 0
	v_addc_co_u32_e32 v69, vcc, 0, v67, vcc
	v_add_co_u32_e32 v70, vcc, s51, v66
	s_mulk_i32 s21, 0xb00
	s_nop 0
	v_addc_co_u32_e32 v71, vcc, 0, v67, vcc
	v_add_co_u32_e32 v72, vcc, s54, v66
	s_add_i32 s21, s21, 0
	s_nop 0
	v_addc_co_u32_e32 v73, vcc, 0, v67, vcc
	v_add_co_u32_e32 v92, vcc, s55, v66
	s_add_i32 s21, s21, 0x20000
	s_nop 0
	v_addc_co_u32_e32 v93, vcc, 0, v67, vcc
	v_add_co_u32_e32 v94, vcc, s56, v66
	s_add_i32 s30, s28, 0x80
	s_nop 0
	v_addc_co_u32_e32 v95, vcc, 0, v67, vcc
	v_add_co_u32_e32 v100, vcc, s57, v66
	s_ashr_i32 s29, s28, 31
	s_nop 0
	v_addc_co_u32_e32 v101, vcc, 0, v67, vcc
	v_add_co_u32_e32 v102, vcc, s58, v66
	s_lshl_b64 s[34:35], s[28:29], 7
	s_nop 0
	v_addc_co_u32_e32 v103, vcc, 0, v67, vcc
	global_load_dword v105, v[66:67], off
	global_load_dword v106, v[68:69], off
	global_load_dword v107, v[70:71], off
	global_load_dword v108, v[72:73], off
	global_load_dword v109, v[92:93], off
	global_load_dword v110, v[94:95], off
	global_load_dword v111, v[100:101], off
	global_load_dword v112, v[102:103], off
	v_add_co_u32_e32 v68, vcc, s59, v66
	s_add_u32 s34, s43, s34
	s_nop 0
	v_addc_co_u32_e32 v69, vcc, 0, v67, vcc
	v_add_co_u32_e32 v70, vcc, s60, v66
	s_addc_u32 s35, s44, s35
	s_nop 0
	v_addc_co_u32_e32 v71, vcc, 0, v67, vcc
	v_add_co_u32_e32 v72, vcc, s61, v66
	s_or_b32 s36, s28, 16
	s_nop 0
	v_addc_co_u32_e32 v73, vcc, 0, v67, vcc
	v_add_co_u32_e32 v92, vcc, s62, v66
	s_ashr_i32 s37, s36, 31
	s_nop 0
	v_addc_co_u32_e32 v93, vcc, 0, v67, vcc
	v_add_co_u32_e32 v94, vcc, s63, v66
	s_nop 1
	v_addc_co_u32_e32 v95, vcc, 0, v67, vcc
	v_add_co_u32_e32 v100, vcc, s64, v66
	s_nop 1
	v_addc_co_u32_e32 v101, vcc, 0, v67, vcc
	v_add_co_u32_e32 v102, vcc, s65, v66
	s_nop 1
	v_addc_co_u32_e32 v103, vcc, 0, v67, vcc
	v_add_co_u32_e32 v66, vcc, s66, v66
	s_nop 1
	v_addc_co_u32_e32 v67, vcc, 0, v67, vcc
	global_load_dword v68, v[68:69], off
	s_nop 0
	global_load_dword v69, v[70:71], off
	s_nop 0
	global_load_dword v70, v[72:73], off
	global_load_dword v71, v[92:93], off
	s_nop 0
	global_load_dword v72, v[94:95], off
	global_load_dword v73, v[100:101], off
	global_load_dword v92, v[102:103], off
	s_nop 0
	global_load_dword v66, v[66:67], off
	s_waitcnt vmcnt(0)
	v_add_f32_e32 v67, v105, v106
	v_lshl_add_u32 v105, v104, 2, s21
	v_add_f32_e32 v93, v107, v108
	v_add_f32_e32 v67, v67, v93
	v_add_f32_e32 v93, v109, v110
	v_add_f32_e32 v94, v111, v112
	v_add_f32_e32 v93, v93, v94
	v_add_f32_e32 v67, v67, v93
	v_add_f32_e32 v68, v68, v69
	v_add_f32_e32 v69, v70, v71
	v_add_f32_e32 v68, v68, v69
	v_add_f32_e32 v69, v72, v73
	v_add_f32_e32 v66, v92, v66
	v_add_f32_e32 v66, v69, v66
	v_add_f32_e32 v66, v68, v66
	v_add_f32_e32 v66, v67, v66
	v_fmamk_f32 v66, v66, 0x3a800000, v99
	v_rsq_f32_e32 v66, v66
	ds_write_b32 v105, v66 offset:2304
	v_or_b32_e32 v66, s30, v104
	v_ashrrev_i32_e32 v67, 31, v66
	v_lshl_add_u64 v[66:67], v[66:67], 2, s[14:15]
	v_add_co_u32_e32 v68, vcc, s50, v66
	s_nop 1
	v_addc_co_u32_e32 v69, vcc, 0, v67, vcc
	v_add_co_u32_e32 v70, vcc, s51, v66
	s_nop 1
	v_addc_co_u32_e32 v71, vcc, 0, v67, vcc
	v_add_co_u32_e32 v72, vcc, s54, v66
	s_nop 1
	v_addc_co_u32_e32 v73, vcc, 0, v67, vcc
	v_add_co_u32_e32 v92, vcc, s55, v66
	s_nop 1
	v_addc_co_u32_e32 v93, vcc, 0, v67, vcc
	v_add_co_u32_e32 v94, vcc, s56, v66
	s_nop 1
	v_addc_co_u32_e32 v95, vcc, 0, v67, vcc
	v_add_co_u32_e32 v100, vcc, s57, v66
	s_nop 1
	v_addc_co_u32_e32 v101, vcc, 0, v67, vcc
	v_add_co_u32_e32 v102, vcc, s58, v66
	s_nop 1
	v_addc_co_u32_e32 v103, vcc, 0, v67, vcc
	global_load_dword v104, v[66:67], off
	global_load_dword v106, v[68:69], off
	global_load_dword v107, v[70:71], off
	global_load_dword v108, v[72:73], off
	global_load_dword v109, v[92:93], off
	global_load_dword v110, v[94:95], off
	global_load_dword v111, v[100:101], off
	global_load_dword v112, v[102:103], off
	v_add_co_u32_e32 v68, vcc, s59, v66
	s_nop 1
	v_addc_co_u32_e32 v69, vcc, 0, v67, vcc
	v_add_co_u32_e32 v70, vcc, s60, v66
	s_nop 1
	v_addc_co_u32_e32 v71, vcc, 0, v67, vcc
	v_add_co_u32_e32 v72, vcc, s61, v66
	s_nop 1
	v_addc_co_u32_e32 v73, vcc, 0, v67, vcc
	v_add_co_u32_e32 v92, vcc, s62, v66
	s_nop 1
	v_addc_co_u32_e32 v93, vcc, 0, v67, vcc
	v_add_co_u32_e32 v94, vcc, s63, v66
	s_nop 1
	v_addc_co_u32_e32 v95, vcc, 0, v67, vcc
	v_add_co_u32_e32 v100, vcc, s64, v66
	s_nop 1
	v_addc_co_u32_e32 v101, vcc, 0, v67, vcc
	v_add_co_u32_e32 v102, vcc, s65, v66
	s_nop 1
	v_addc_co_u32_e32 v103, vcc, 0, v67, vcc
	v_add_co_u32_e32 v66, vcc, s66, v66
	s_nop 1
	v_addc_co_u32_e32 v67, vcc, 0, v67, vcc
	global_load_dword v68, v[68:69], off
	s_nop 0
	global_load_dword v69, v[70:71], off
	s_nop 0
	global_load_dword v70, v[72:73], off
	global_load_dword v71, v[92:93], off
	s_nop 0
	global_load_dword v72, v[94:95], off
	global_load_dword v73, v[100:101], off
	global_load_dword v92, v[102:103], off
	s_nop 0
	global_load_dword v66, v[66:67], off
	v_and_b32_e32 v101, 15, v82
	v_mov_b32_e32 v103, s21
	v_mov_b32_e32 v95, v83
	s_waitcnt vmcnt(14)
	v_add_f32_e32 v67, v104, v106
	s_waitcnt vmcnt(12)
	v_add_f32_e32 v93, v107, v108
	v_add_f32_e32 v67, v67, v93
	s_waitcnt vmcnt(10)
	v_add_f32_e32 v93, v109, v110
	v_lshl_add_u32 v108, v101, 2, s21
	s_waitcnt vmcnt(8)
	v_add_f32_e32 v94, v111, v112
	v_add_f32_e32 v93, v93, v94
	v_add_f32_e32 v67, v67, v93
	v_bfe_u32 v94, v82, 3, 3
	v_mul_u32_u24_e32 v102, 0x90, v94
	v_mov_b32_e32 v93, v83
	s_waitcnt vmcnt(6)
	v_add_f32_e32 v68, v68, v69
	s_waitcnt vmcnt(4)
	v_add_f32_e32 v69, v70, v71
	v_add_f32_e32 v68, v68, v69
	s_waitcnt vmcnt(2)
	v_add_f32_e32 v69, v72, v73
	s_waitcnt vmcnt(0)
	v_add_f32_e32 v66, v92, v66
	v_add_f32_e32 v66, v69, v66
	v_add_f32_e32 v66, v68, v66
	v_add_f32_e32 v66, v67, v66
	v_fmamk_f32 v66, v66, 0x3a800000, v99
	v_rsq_f32_e32 v66, v66
	ds_write_b32 v105, v66 offset:2560
	v_lshlrev_b32_e32 v66, 1, v82
	v_and_b32_e32 v100, 0x60, v66
	global_load_dwordx4 v[70:73], v100, s[10:11]
	global_load_dwordx4 v[66:69], v100, s[10:11] offset:16
	ds_read_b32 v108, v108 offset:2304
	v_lshlrev_b32_e32 v82, 4, v82
	v_and_b32_e32 v92, 0x70, v82
	v_add3_u32 v109, s21, v102, v92
	v_mad_u32_u24 v102, v101, s67, v103
	v_add_u32_e32 v114, v102, v100
	v_mad_i32_i24 v115, v101, s68, v102
	v_lshlrev_b32_e32 v82, 7, v94
	v_or_b32_e32 v94, 0x400, v82
	v_lshl_add_u64 v[100:101], s[34:35], 0, v[82:83]
	v_lshl_add_u64 v[102:103], s[34:35], 0, v[94:95]
	v_lshl_add_u64 v[100:101], v[100:101], 0, v[92:93]
	v_lshl_add_u64 v[102:103], v[102:103], 0, v[92:93]
	s_lshl_b64 s[34:35], s[36:37], 7
	s_add_u32 s34, s43, s34
	s_addc_u32 s35, s44, s35
	s_or_b32 s36, s28, 32
	s_ashr_i32 s37, s36, 31
	v_lshl_add_u64 v[104:105], s[34:35], 0, v[82:83]
	v_lshl_add_u64 v[106:107], s[34:35], 0, v[94:95]
	s_lshl_b64 s[34:35], s[36:37], 7
	s_add_u32 s34, s43, s34
	s_addc_u32 s35, s44, s35
	s_or_b32 s36, s28, 48
	v_lshl_add_u64 v[104:105], v[104:105], 0, v[92:93]
	v_lshl_add_u64 v[110:111], s[34:35], 0, v[82:83]
	v_lshl_add_u64 v[112:113], s[34:35], 0, v[94:95]
	s_ashr_i32 s37, s36, 31
	v_lshl_add_u64 v[106:107], v[106:107], 0, v[92:93]
	v_lshl_add_u64 v[110:111], v[110:111], 0, v[92:93]
	v_lshl_add_u64 v[112:113], v[112:113], 0, v[92:93]
	s_lshl_b64 s[34:35], s[36:37], 7
	s_add_u32 s34, s43, s34
	s_addc_u32 s35, s44, s35
	s_ashr_i32 s31, s30, 31
	s_lshl_b64 s[30:31], s[30:31], 7
	s_add_u32 s30, s43, s30
	s_addc_u32 s31, s44, s31
	s_waitcnt vmcnt(1) lgkmcnt(0)
	v_pk_fma_f32 v[64:65], v[64:65], v[108:109], v[72:73] op_sel_hi:[1,0,1]
	v_pk_fma_f32 v[62:63], v[62:63], v[108:109], v[70:71] op_sel_hi:[1,0,1]
	s_waitcnt vmcnt(0)
	v_pk_fma_f32 v[60:61], v[60:61], v[108:109], v[68:69] op_sel_hi:[1,0,1]
	v_pk_fma_f32 v[58:59], v[58:59], v[108:109], v[66:67] op_sel_hi:[1,0,1]
	ds_write_b128 v114, v[62:65]
	ds_write_b128 v114, v[58:61] offset:16
	ds_read_b32 v108, v115 offset:2368
	ds_read_b128 v[58:61], v109
	ds_read_b128 v[62:65], v109 offset:1152
	s_waitcnt lgkmcnt(2)
	v_pk_fma_f32 v[56:57], v[56:57], v[108:109], v[72:73] op_sel_hi:[1,0,1]
	v_pk_fma_f32 v[54:55], v[54:55], v[108:109], v[70:71] op_sel_hi:[1,0,1]
	v_pk_fma_f32 v[52:53], v[52:53], v[108:109], v[68:69] op_sel_hi:[1,0,1]
	v_pk_fma_f32 v[50:51], v[50:51], v[108:109], v[66:67] op_sel_hi:[1,0,1]
	ds_write_b128 v114, v[54:57]
	ds_write_b128 v114, v[50:53] offset:16
	ds_read_b32 v108, v115 offset:2432
	s_waitcnt lgkmcnt(4)
	global_store_dwordx4 v[100:101], v[58:61], off sc1
	s_waitcnt lgkmcnt(3)
	global_store_dwordx4 v[102:103], v[62:65], off sc1
	ds_read_b128 v[50:53], v109
	ds_read_b128 v[54:57], v109 offset:1152
	s_waitcnt lgkmcnt(2)
	v_pk_fma_f32 v[48:49], v[48:49], v[108:109], v[72:73] op_sel_hi:[1,0,1]
	v_pk_fma_f32 v[46:47], v[46:47], v[108:109], v[70:71] op_sel_hi:[1,0,1]
	v_pk_fma_f32 v[44:45], v[44:45], v[108:109], v[68:69] op_sel_hi:[1,0,1]
	v_pk_fma_f32 v[42:43], v[42:43], v[108:109], v[66:67] op_sel_hi:[1,0,1]
	ds_write_b128 v114, v[46:49]
	ds_write_b128 v114, v[42:45] offset:16
	ds_read_b128 v[42:45], v109
	ds_read_b128 v[46:49], v109 offset:1152
	ds_read_b32 v58, v115 offset:2496
	s_waitcnt lgkmcnt(6)
	global_store_dwordx4 v[104:105], v[50:53], off sc1
	s_waitcnt lgkmcnt(5)
	global_store_dwordx4 v[106:107], v[54:57], off sc1
	s_waitcnt lgkmcnt(2)
	global_store_dwordx4 v[110:111], v[42:45], off sc1
	s_waitcnt lgkmcnt(1)
	global_store_dwordx4 v[112:113], v[46:49], off sc1
	s_waitcnt lgkmcnt(0)
	v_pk_fma_f32 v[40:41], v[40:41], v[58:59], v[72:73] op_sel_hi:[1,0,1]
	v_pk_fma_f32 v[38:39], v[38:39], v[58:59], v[70:71] op_sel_hi:[1,0,1]
	v_pk_fma_f32 v[36:37], v[36:37], v[58:59], v[68:69] op_sel_hi:[1,0,1]
	v_pk_fma_f32 v[34:35], v[34:35], v[58:59], v[66:67] op_sel_hi:[1,0,1]
	ds_write_b128 v114, v[38:41]
	ds_write_b128 v114, v[34:37] offset:16
	ds_read_b128 v[34:37], v109
	ds_read_b128 v[38:41], v109 offset:1152
	ds_read_b32 v44, v115 offset:2560
	v_lshl_add_u64 v[42:43], s[34:35], 0, v[82:83]
	v_lshl_add_u64 v[42:43], v[42:43], 0, v[92:93]
	s_waitcnt lgkmcnt(2)
	global_store_dwordx4 v[42:43], v[34:37], off sc1
	s_waitcnt lgkmcnt(0)
	v_pk_fma_f32 v[32:33], v[32:33], v[44:45], v[72:73] op_sel_hi:[1,0,1]
	v_lshl_add_u64 v[34:35], s[34:35], 0, v[94:95]
	v_lshl_add_u64 v[34:35], v[34:35], 0, v[92:93]
	v_pk_fma_f32 v[30:31], v[30:31], v[44:45], v[70:71] op_sel_hi:[1,0,1]
	global_store_dwordx4 v[34:35], v[38:41], off sc1
	v_pk_fma_f32 v[28:29], v[28:29], v[44:45], v[68:69] op_sel_hi:[1,0,1]
	v_pk_fma_f32 v[26:27], v[26:27], v[44:45], v[66:67] op_sel_hi:[1,0,1]
	ds_write_b128 v114, v[30:33]
	ds_write_b128 v114, v[26:29] offset:16
	ds_read_b128 v[26:29], v109
	ds_read_b128 v[30:33], v109 offset:1152
	ds_read_b32 v36, v115 offset:2624
	v_lshl_add_u64 v[34:35], s[30:31], 0, v[82:83]
	v_lshl_add_u64 v[34:35], v[34:35], 0, v[92:93]
	s_waitcnt lgkmcnt(2)
	global_store_dwordx4 v[34:35], v[26:29], off sc1
	s_waitcnt lgkmcnt(0)
	v_pk_fma_f32 v[24:25], v[24:25], v[36:37], v[72:73] op_sel_hi:[1,0,1]
	v_lshl_add_u64 v[26:27], s[30:31], 0, v[94:95]
	s_add_i32 s30, s28, 0x90
	v_lshl_add_u64 v[26:27], v[26:27], 0, v[92:93]
	v_pk_fma_f32 v[22:23], v[22:23], v[36:37], v[70:71] op_sel_hi:[1,0,1]
	s_ashr_i32 s31, s30, 31
	global_store_dwordx4 v[26:27], v[30:33], off sc1
	v_pk_fma_f32 v[20:21], v[20:21], v[36:37], v[68:69] op_sel_hi:[1,0,1]
	v_pk_fma_f32 v[18:19], v[18:19], v[36:37], v[66:67] op_sel_hi:[1,0,1]
	s_lshl_b64 s[30:31], s[30:31], 7
	ds_write_b128 v114, v[22:25]
	ds_write_b128 v114, v[18:21] offset:16
	s_add_u32 s30, s43, s30
	ds_read_b128 v[18:21], v109
	ds_read_b128 v[22:25], v109 offset:1152
	ds_read_b32 v28, v115 offset:2688
	s_addc_u32 s31, s44, s31
	v_lshl_add_u64 v[26:27], s[30:31], 0, v[82:83]
	v_lshl_add_u64 v[26:27], v[26:27], 0, v[92:93]
	s_waitcnt lgkmcnt(2)
	global_store_dwordx4 v[26:27], v[18:21], off sc1
	s_waitcnt lgkmcnt(0)
	v_pk_fma_f32 v[16:17], v[16:17], v[28:29], v[72:73] op_sel_hi:[1,0,1]
	v_pk_fma_f32 v[14:15], v[14:15], v[28:29], v[70:71] op_sel_hi:[1,0,1]
	v_lshl_add_u64 v[18:19], s[30:31], 0, v[94:95]
	s_add_i32 s30, s28, 0xa0
	v_lshl_add_u64 v[18:19], v[18:19], 0, v[92:93]
	s_ashr_i32 s31, s30, 31
	global_store_dwordx4 v[18:19], v[22:25], off sc1
	v_pk_fma_f32 v[12:13], v[12:13], v[28:29], v[68:69] op_sel_hi:[1,0,1]
	v_pk_fma_f32 v[10:11], v[10:11], v[28:29], v[66:67] op_sel_hi:[1,0,1]
	s_lshl_b64 s[30:31], s[30:31], 7
	ds_write_b128 v114, v[14:17]
	ds_write_b128 v114, v[10:13] offset:16
	s_add_u32 s30, s43, s30
	ds_read_b128 v[10:13], v109
	ds_read_b128 v[14:17], v109 offset:1152
	ds_read_b32 v20, v115 offset:2752
	s_addc_u32 s31, s44, s31
	v_lshl_add_u64 v[18:19], s[30:31], 0, v[82:83]
	v_lshl_add_u64 v[18:19], v[18:19], 0, v[92:93]
	s_waitcnt lgkmcnt(2)
	global_store_dwordx4 v[18:19], v[10:13], off sc1
	s_waitcnt lgkmcnt(0)
	v_pk_fma_f32 v[8:9], v[8:9], v[20:21], v[72:73] op_sel_hi:[1,0,1]
	v_pk_fma_f32 v[6:7], v[6:7], v[20:21], v[70:71] op_sel_hi:[1,0,1]
	v_lshl_add_u64 v[10:11], s[30:31], 0, v[94:95]
	v_lshl_add_u64 v[10:11], v[10:11], 0, v[92:93]
	s_addk_i32 s28, 0xb0
	global_store_dwordx4 v[10:11], v[14:17], off sc1
	v_pk_fma_f32 v[4:5], v[4:5], v[20:21], v[68:69] op_sel_hi:[1,0,1]
	v_pk_fma_f32 v[2:3], v[2:3], v[20:21], v[66:67] op_sel_hi:[1,0,1]
	s_ashr_i32 s29, s28, 31
	ds_write_b128 v114, v[6:9]
	ds_write_b128 v114, v[2:5] offset:16
	s_lshl_b64 s[28:29], s[28:29], 7
	ds_read_b128 v[2:5], v109
	ds_read_b128 v[6:9], v109 offset:1152
	s_add_u32 s28, s43, s28
	s_addc_u32 s29, s44, s29
	v_lshl_add_u64 v[10:11], s[28:29], 0, v[82:83]
	v_lshl_add_u64 v[10:11], v[10:11], 0, v[92:93]
	s_waitcnt lgkmcnt(1)
	global_store_dwordx4 v[10:11], v[2:5], off sc1
	s_nop 1
	v_lshl_add_u64 v[2:3], s[28:29], 0, v[94:95]
	v_lshl_add_u64 v[2:3], v[2:3], 0, v[92:93]
	s_waitcnt lgkmcnt(0)
	global_store_dwordx4 v[2:3], v[6:9], off sc1
	s_andn2_b64 vcc, exec, s[6:7]
	s_mov_b64 s[6:7], -1
	s_cbranch_vccnz .LBB0_564

.LBB0_1094:
	s_or_b64 exec, exec, s[10:11]
	v_sub_f32_e32 v2, v47, v45
	v_mul_f32_e32 v2, 0x3fb8aa3b, v2
	v_exp_f32_e32 v4, v2
	v_sub_f32_e32 v2, v49, v45
	v_mul_f32_e32 v2, 0x3fb8aa3b, v2
	v_exp_f32_e32 v5, v2
	v_sub_f32_e32 v2, v50, v45
	v_mul_f32_e32 v2, 0x3fb8aa3b, v2
	v_exp_f32_e32 v3, v2
	v_add_f32_e32 v2, 1.0, v4
	v_add_f32_e32 v2, v2, v5
	v_add_f32_e32 v2, v2, v3
	v_div_scale_f32 v6, s[10:11], v2, v2, 1.0
	v_rcp_f32_e32 v7, v6
	s_nop 0
	v_fma_f32 v8, -v6, v7, 1.0
	v_fmac_f32_e32 v7, v8, v7
	v_div_scale_f32 v8, vcc, 1.0, v2, 1.0
	v_mul_f32_e32 v9, v8, v7
	v_fma_f32 v10, -v6, v9, v8
	v_fmac_f32_e32 v9, v10, v7
	v_fma_f32 v6, -v6, v9, v8
	v_div_fmas_f32 v6, v6, v7, v9
	v_div_fixup_f32 v2, v6, v2, 1.0
	v_lshlrev_b32_e32 v6, 16, v48
	v_lshlrev_b32_e32 v7, 24, v30
	v_lshl_or_b32 v6, v46, 8, v6
	v_or3_b32 v8, v6, v7, v44
	v_lshl_add_u64 v[6:7], v[38:39], 2, s[18:19]
	global_store_dword v[6:7], v8, off sc1
	v_pk_mul_f32 v[6:7], v[4:5], v[2:3] op_sel_hi:[1,0]
	v_mul_f32_e32 v5, v3, v2
	v_lshl_add_u64 v[8:9], v[38:39], 4, s[20:21]
	v_mov_b32_e32 v3, v6
	v_mov_b32_e32 v4, v7
	global_store_dwordx4 v[8:9], v[2:5], off sc1
	s_nop 1
	v_lshl_add_u32 v2, v44, 2, 0
	ds_add_u32 v2, v42
	v_lshl_add_u32 v2, v46, 2, 0
	ds_add_u32 v2, v42
	v_lshl_add_u32 v2, v48, 2, 0
	ds_add_u32 v2, v42
	v_lshl_add_u32 v2, v30, 2, 0
	ds_add_u32 v2, v42
.LBB0_1095:
	s_or_b64 exec, exec, s[26:27]
	s_waitcnt lgkmcnt(0)
	s_barrier
	s_and_saveexec_b64 s[10:11], s[6:7]
	s_cbranch_execz .LBB0_582
	ds_read_b32 v4, v40
	v_lshl_add_u32 v2, s4, 5, v1
	v_ashrrev_i32_e32 v3, 31, v2
	v_lshl_add_u64 v[2:3], v[2:3], 2, s[22:23]
	s_waitcnt lgkmcnt(0)
	global_store_dword v[2:3], v4, off sc1
	s_branch .LBB0_582

.LBB0_1379:
	s_andn2_saveexec_b64 s[0:1], s[10:11]
	s_cbranch_execz .LBB0_1399
	s_mov_b64 s[10:11], exec
	s_waitcnt lgkmcnt(0)
	s_waitcnt vmcnt(0)
	v_mbcnt_lo_u32_b32 v2, s10, 0
	v_mbcnt_hi_u32_b32 v2, s11, v2
	v_cmp_eq_u32_e32 vcc, 0, v2
	s_and_saveexec_b64 s[12:13], vcc
	s_cbranch_execz .LBB0_1382
	s_bcnt1_i32_b64 s0, s[10:11]
	v_mov_b32_e32 v3, 0x7000
	v_mov_b32_e32 v4, s0
	global_atomic_add v3, v3, v4, s[52:53] offset:1024 sc0

.LBB0_1401:
	v_ashrrev_i32_e32 v5, 31, v4
	v_lshlrev_b64 v[34:35], 2, v[4:5]
	v_lshl_add_u64 v[36:37], s[30:31], 0, v[34:35]
	global_store_dword v[36:37], v7, off sc1
	v_lshl_add_u64 v[6:7], s[36:37], 0, v[34:35]
	global_store_dword v[6:7], v22, off sc1
	v_lshl_add_u64 v[6:7], s[38:39], 0, v[34:35]
	v_mov_b32_e32 v9, v26
	v_mov_b32_e32 v11, v4
	v_lshl_add_u64 v[4:5], v[24:25], 2, s[28:29]
	global_store_dword v[6:7], v23, off sc1
	global_store_dwordx4 v[4:5], v[8:11], off sc1

.LBB0_1419:
	s_or_b64 exec, exec, s[18:19]
	s_cmp_eq_u32 s55, 0
	s_cselect_b64 s[18:19], -1, 0
	s_and_b64 s[20:21], s[18:19], s[12:13]
	s_and_saveexec_b64 s[18:19], s[20:21]
	s_cbranch_execz .LBB0_1421
	ds_read_b32 v1, v21 offset:2304
	s_waitcnt lgkmcnt(0)
	global_store_dword v[18:19], v1, off sc1

.LBB0_1438:
	s_waitcnt vmcnt(14)
	v_add_f32_e32 v1, v9, v11
	s_waitcnt vmcnt(12)
	v_add_f32_e32 v9, v23, v35
	v_add_f32_e32 v1, v1, v9
	s_waitcnt vmcnt(10)
	v_add_f32_e32 v9, v26, v36
	s_waitcnt vmcnt(8)
	v_add_f32_e32 v11, v37, v39
	v_add_f32_e32 v9, v9, v11
	v_add_f32_e32 v1, v1, v9
	s_waitcnt vmcnt(6)
	v_add_f32_e32 v9, v27, v38
	s_waitcnt vmcnt(4)
	v_add_f32_e32 v11, v40, v42
	v_add_f32_e32 v9, v9, v11
	s_waitcnt vmcnt(2)
	v_add_f32_e32 v11, v41, v43
	s_waitcnt vmcnt(0)
	v_add_f32_e32 v23, v44, v45
	v_add_f32_e32 v11, v11, v23
	v_add_f32_e32 v9, v9, v11
	v_add_f32_e32 v1, v1, v9
	v_ashrrev_i32_e32 v9, 31, v8
	v_lshlrev_b64 v[26:27], 2, v[8:9]
	v_lshl_add_u64 v[36:37], s[30:31], 0, v[26:27]
	global_store_dword v[36:37], v4, off sc1
	v_bfe_u32 v4, v33, 8, 8
	v_fmamk_f32 v1, v1, 0x3a800000, v31
	v_lshl_add_u32 v9, v4, 2, 0
	v_rsq_f32_e32 v23, v1
	ds_read_b32 v1, v9 offset:2560
	v_lshl_add_u64 v[36:37], s[36:37], 0, v[26:27]
	v_lshl_add_u64 v[26:27], s[38:39], 0, v[26:27]
	global_store_dword v[26:27], v23, off sc1
	s_and_b64 vcc, exec, s[20:21]
	s_waitcnt lgkmcnt(0)
	v_add_u32_e32 v26, v1, v10
	global_store_dword v[36:37], v22, off sc1
	s_cbranch_vccnz .LBB0_1449
	s_and_b64 vcc, exec, s[18:19]
	s_cbranch_vccnz .LBB0_1446
	s_andn2_b64 vcc, exec, s[46:47]
	s_cbranch_vccnz .LBB0_1472
	s_mov_b32 s65, 1
	v_mov_b32_e32 v1, 0
	s_mov_b32 s64, 0
	s_mov_b32 s56, s5

.LBB0_1449:
	v_ashrrev_i32_e32 v27, 31, v26
	v_lshlrev_b64 v[10:11], 2, v[26:27]
	v_bfe_u32 v1, v33, 16, 8
	v_lshl_add_u64 v[36:37], s[30:31], 0, v[10:11]
	v_lshl_add_u32 v4, v1, 2, 0
	global_store_dword v[36:37], v5, off sc1
	ds_read_b32 v5, v4 offset:2560
	v_lshl_add_u64 v[36:37], s[36:37], 0, v[10:11]
	v_lshl_add_u64 v[10:11], s[38:39], 0, v[10:11]
	global_store_dword v[10:11], v23, off sc1
	s_and_b64 vcc, exec, s[20:21]
	s_waitcnt lgkmcnt(0)
	v_add_u32_e32 v10, v5, v3
	global_store_dword v[36:37], v22, off sc1
	s_cbranch_vccnz .LBB0_1460
	s_and_b64 vcc, exec, s[18:19]
	s_cbranch_vccnz .LBB0_1457
	s_andn2_b64 vcc, exec, s[46:47]
	s_cbranch_vccnz .LBB0_1473
	s_mov_b32 s65, 1
	v_mov_b32_e32 v3, 0
	s_mov_b32 s64, 0
	s_mov_b32 s56, s5

.LBB0_1460:
	v_ashrrev_i32_e32 v11, 31, v10
	v_lshlrev_b64 v[36:37], 2, v[10:11]
	v_lshl_add_u64 v[4:5], s[30:31], 0, v[36:37]
	v_lshrrev_b32_e32 v3, 24, v33
	global_store_dword v[4:5], v6, off sc1
	v_lshl_add_u32 v5, v3, 2, 0
	ds_read_b32 v1, v5 offset:2560
	v_lshl_add_u64 v[38:39], s[36:37], 0, v[36:37]
	v_lshl_add_u64 v[36:37], s[38:39], 0, v[36:37]
	s_and_b64 vcc, exec, s[20:21]
	global_store_dword v[38:39], v22, off sc1
	s_waitcnt lgkmcnt(0)
	v_add_u32_e32 v4, v1, v34
	global_store_dword v[36:37], v23, off sc1
	s_cbranch_vccnz .LBB0_1401
	s_and_b64 vcc, exec, s[18:19]
	s_cbranch_vccnz .LBB0_1468
	s_andn2_b64 vcc, exec, s[46:47]
	s_cbranch_vccnz .LBB0_1474
	s_mov_b32 s19, 1
	v_mov_b32_e32 v1, 0
	s_mov_b32 s18, 0
	s_mov_b32 s20, s5

.LBB0_1683:
	s_or_b64 exec, exec, s[6:7]
	v_mov_b32_e32 v2, v0
	s_lshr_b32 s3, s95, 3
	s_waitcnt lgkmcnt(0)
	s_barrier
	s_mul_i32 s3, s3, s64
	v_readfirstlane_b32 s0, v2
	v_readlane_b32 s4, v254, 12
	s_ashr_i32 s1, s0, 6
	s_and_b32 s0, s95, 7
	s_add_i32 s3, s3, s4
	s_cmp_eq_u32 s0, 0
	s_cselect_b32 s0, s3, s2
	s_lshl_b32 s63, s0, 3
	s_add_i32 s0, s1, s63
	s_lshl_b32 s50, s95, 3
	s_cmp_lt_i32 s0, 0x10000
	s_cbranch_scc0 .LBB0_1686
	s_load_dwordx2 s[4:5], s[90:91], 0xc8
	v_and_b32_e32 v1, 63, v0
	v_lshlrev_b32_e32 v2, 4, v1
	v_lshlrev_b32_e32 v3, 3, v1
	v_mov_b32_e32 v5, 0
	v_mov_b32_e32 v6, 0x358637bd
	s_mov_b32 s16, 0x3e000000
	s_mov_b32 s17, 0
	s_waitcnt lgkmcnt(0)
	s_add_u32 s6, s4, 0xf00000
	s_addc_u32 s7, s5, 0
	s_add_u32 s8, s4, 0x1ec00000
	s_addc_u32 s9, s5, 0
	s_add_u32 s10, s4, 0x2ec00000
	s_addc_u32 s11, s5, 0
	s_add_u32 s14, s4, 0x5fc00000
	s_addc_u32 s15, s5, 0
	s_add_u32 s30, s4, 0x6bc00000
	s_addc_u32 s31, s5, 0
	s_add_i32 s1, s0, s50
	s_min_i32 s3, s0, 0xffff
	s_lshl_b32 s3, s3, 4
	s_add_u32 s34, s6, s3
	s_addc_u32 s35, s7, 0
	global_load_dwordx4 v[12:15], v5, s[34:35]
	s_min_i32 s3, s1, 0xffff
	s_lshl_b32 s3, s3, 4
	s_add_u32 s36, s6, s3
	s_addc_u32 s37, s7, 0
	global_load_dwordx4 v[16:19], v5, s[36:37]
	s_waitcnt vmcnt(1)
	v_readfirstlane_b32 s56, v12
	v_readfirstlane_b32 s57, v13
	v_readfirstlane_b32 s58, v14
	v_readfirstlane_b32 s59, v15
	s_min_i32 s3, s0, 0xffff
	s_lshl_b32 s3, s3, 11
	s_add_u32 s60, s8, s3
	s_addc_u32 s61, s9, 0
	global_load_dwordx4 v[20:23], v2, s[60:61]
	global_load_dwordx4 v[24:27], v2, s[60:61] offset:1024
	s_lshl_b32 s3, s56, 10
	s_add_u32 s68, s10, s3
	s_addc_u32 s69, s11, 0
	global_load_dwordx2 v[28:29], v3, s[68:69]
	global_load_dwordx2 v[36:37], v3, s[68:69] offset:512
	s_lshl_b32 s3, s57, 10
	s_add_u32 s72, s10, s3
	s_addc_u32 s73, s11, 0
	global_load_dwordx2 v[30:31], v3, s[72:73]
	global_load_dwordx2 v[38:39], v3, s[72:73] offset:512
	s_lshl_b32 s3, s58, 10
	s_add_u32 s74, s10, s3
	s_addc_u32 s75, s11, 0
	global_load_dwordx2 v[32:33], v3, s[74:75]
	global_load_dwordx2 v[40:41], v3, s[74:75] offset:512
	s_lshl_b32 s3, s59, 10
	s_add_u32 s78, s10, s3
	s_addc_u32 s79, s11, 0
	global_load_dwordx2 v[34:35], v3, s[78:79]
	global_load_dwordx2 v[42:43], v3, s[78:79] offset:512
	s_add_i32 s1, s0, s50
	s_add_i32 s13, s1, s50
	s_min_i32 s3, s13, 0xffff
	s_lshl_b32 s3, s3, 4
	s_add_u32 s34, s6, s3
	s_addc_u32 s35, s7, 0
	global_load_dwordx4 v[12:15], v5, s[34:35]
	s_waitcnt vmcnt(11)
	v_readfirstlane_b32 s56, v16
	v_readfirstlane_b32 s57, v17
	v_readfirstlane_b32 s58, v18
	v_readfirstlane_b32 s59, v19
	s_min_i32 s3, s1, 0xffff
	s_lshl_b32 s3, s3, 11
	s_add_u32 s60, s8, s3
	s_addc_u32 s61, s9, 0
	global_load_dwordx4 v[48:51], v2, s[60:61]
	global_load_dwordx4 v[52:55], v2, s[60:61] offset:1024
	s_lshl_b32 s3, s56, 10
	s_add_u32 s68, s10, s3
	s_addc_u32 s69, s11, 0
	global_load_dwordx2 v[56:57], v3, s[68:69]
	global_load_dwordx2 v[64:65], v3, s[68:69] offset:512
	s_lshl_b32 s3, s57, 10
	s_add_u32 s72, s10, s3
	s_addc_u32 s73, s11, 0
	global_load_dwordx2 v[58:59], v3, s[72:73]
	global_load_dwordx2 v[66:67], v3, s[72:73] offset:512
	s_lshl_b32 s3, s58, 10
	s_add_u32 s74, s10, s3
	s_addc_u32 s75, s11, 0
	global_load_dwordx2 v[60:61], v3, s[74:75]
	global_load_dwordx2 v[68:69], v3, s[74:75] offset:512
	s_lshl_b32 s3, s59, 10
	s_add_u32 s78, s10, s3
	s_addc_u32 s79, s11, 0
	global_load_dwordx2 v[62:63], v3, s[78:79]
	global_load_dwordx2 v[70:71], v3, s[78:79] offset:512
	s_waitcnt vmcnt(11)
	v_lshlrev_b32_e32 v80, 16, v20
	v_and_b32_e32 v81, 0xffff0000, v20
	v_lshlrev_b32_e32 v82, 16, v21
	v_and_b32_e32 v83, 0xffff0000, v21
	v_lshlrev_b32_e32 v84, 16, v22
	v_and_b32_e32 v85, 0xffff0000, v22
	v_lshlrev_b32_e32 v86, 16, v23
	v_and_b32_e32 v87, 0xffff0000, v23
	v_lshlrev_b32_e32 v88, 16, v24
	v_and_b32_e32 v89, 0xffff0000, v24
	v_lshlrev_b32_e32 v90, 16, v25
	v_and_b32_e32 v91, 0xffff0000, v25
	v_lshlrev_b32_e32 v92, 16, v26
	v_and_b32_e32 v93, 0xffff0000, v26
	v_lshlrev_b32_e32 v94, 16, v27
	v_and_b32_e32 v95, 0xffff0000, v27
	v_cvt_pk_f32_fp8_e32 v[96:97], v28
	v_cvt_pk_f32_fp8_sdwa v[98:99], v28 src0_sel:WORD_1
	v_cvt_pk_f32_fp8_e32 v[100:101], v29
	v_cvt_pk_f32_fp8_sdwa v[102:103], v29 src0_sel:WORD_1
	v_cvt_pk_f32_fp8_e32 v[104:105], v36
	v_cvt_pk_f32_fp8_sdwa v[106:107], v36 src0_sel:WORD_1
	v_cvt_pk_f32_fp8_e32 v[108:109], v37
	v_cvt_pk_f32_fp8_sdwa v[110:111], v37 src0_sel:WORD_1
	v_pk_fma_f32 v[80:81], v[96:97], s[16:17], v[80:81] op_sel_hi:[1,0,1]
	v_pk_fma_f32 v[82:83], v[98:99], s[16:17], v[82:83] op_sel_hi:[1,0,1]
	v_pk_fma_f32 v[84:85], v[100:101], s[16:17], v[84:85] op_sel_hi:[1,0,1]
	v_pk_fma_f32 v[86:87], v[102:103], s[16:17], v[86:87] op_sel_hi:[1,0,1]
	v_pk_fma_f32 v[88:89], v[104:105], s[16:17], v[88:89] op_sel_hi:[1,0,1]
	v_pk_fma_f32 v[90:91], v[106:107], s[16:17], v[90:91] op_sel_hi:[1,0,1]
	v_pk_fma_f32 v[92:93], v[108:109], s[16:17], v[92:93] op_sel_hi:[1,0,1]
	v_pk_fma_f32 v[94:95], v[110:111], s[16:17], v[94:95] op_sel_hi:[1,0,1]
	v_cvt_pk_f32_fp8_e32 v[96:97], v30
	v_cvt_pk_f32_fp8_sdwa v[98:99], v30 src0_sel:WORD_1
	v_cvt_pk_f32_fp8_e32 v[100:101], v31
	v_cvt_pk_f32_fp8_sdwa v[102:103], v31 src0_sel:WORD_1
	v_cvt_pk_f32_fp8_e32 v[104:105], v38
	v_cvt_pk_f32_fp8_sdwa v[106:107], v38 src0_sel:WORD_1
	v_cvt_pk_f32_fp8_e32 v[108:109], v39
	v_cvt_pk_f32_fp8_sdwa v[110:111], v39 src0_sel:WORD_1
	v_pk_fma_f32 v[80:81], v[96:97], s[16:17], v[80:81] op_sel_hi:[1,0,1]
	v_pk_fma_f32 v[82:83], v[98:99], s[16:17], v[82:83] op_sel_hi:[1,0,1]
	v_pk_fma_f32 v[84:85], v[100:101], s[16:17], v[84:85] op_sel_hi:[1,0,1]
	v_pk_fma_f32 v[86:87], v[102:103], s[16:17], v[86:87] op_sel_hi:[1,0,1]
	v_pk_fma_f32 v[88:89], v[104:105], s[16:17], v[88:89] op_sel_hi:[1,0,1]
	v_pk_fma_f32 v[90:91], v[106:107], s[16:17], v[90:91] op_sel_hi:[1,0,1]
	v_pk_fma_f32 v[92:93], v[108:109], s[16:17], v[92:93] op_sel_hi:[1,0,1]
	v_pk_fma_f32 v[94:95], v[110:111], s[16:17], v[94:95] op_sel_hi:[1,0,1]
	v_cvt_pk_f32_fp8_e32 v[96:97], v32
	v_cvt_pk_f32_fp8_sdwa v[98:99], v32 src0_sel:WORD_1
	v_cvt_pk_f32_fp8_e32 v[100:101], v33
	v_cvt_pk_f32_fp8_sdwa v[102:103], v33 src0_sel:WORD_1
	v_cvt_pk_f32_fp8_e32 v[104:105], v40
	v_cvt_pk_f32_fp8_sdwa v[106:107], v40 src0_sel:WORD_1
	v_cvt_pk_f32_fp8_e32 v[108:109], v41
	v_cvt_pk_f32_fp8_sdwa v[110:111], v41 src0_sel:WORD_1
	v_pk_fma_f32 v[80:81], v[96:97], s[16:17], v[80:81] op_sel_hi:[1,0,1]
	v_pk_fma_f32 v[82:83], v[98:99], s[16:17], v[82:83] op_sel_hi:[1,0,1]
	v_pk_fma_f32 v[84:85], v[100:101], s[16:17], v[84:85] op_sel_hi:[1,0,1]
	v_pk_fma_f32 v[86:87], v[102:103], s[16:17], v[86:87] op_sel_hi:[1,0,1]
	v_pk_fma_f32 v[88:89], v[104:105], s[16:17], v[88:89] op_sel_hi:[1,0,1]
	v_pk_fma_f32 v[90:91], v[106:107], s[16:17], v[90:91] op_sel_hi:[1,0,1]
	v_pk_fma_f32 v[92:93], v[108:109], s[16:17], v[92:93] op_sel_hi:[1,0,1]
	v_pk_fma_f32 v[94:95], v[110:111], s[16:17], v[94:95] op_sel_hi:[1,0,1]
	v_cvt_pk_f32_fp8_e32 v[96:97], v34
	v_cvt_pk_f32_fp8_sdwa v[98:99], v34 src0_sel:WORD_1
	v_cvt_pk_f32_fp8_e32 v[100:101], v35
	v_cvt_pk_f32_fp8_sdwa v[102:103], v35 src0_sel:WORD_1
	v_cvt_pk_f32_fp8_e32 v[104:105], v42
	v_cvt_pk_f32_fp8_sdwa v[106:107], v42 src0_sel:WORD_1
	v_cvt_pk_f32_fp8_e32 v[108:109], v43
	v_cvt_pk_f32_fp8_sdwa v[110:111], v43 src0_sel:WORD_1
	v_pk_fma_f32 v[80:81], v[96:97], s[16:17], v[80:81] op_sel_hi:[1,0,1]
	v_pk_fma_f32 v[82:83], v[98:99], s[16:17], v[82:83] op_sel_hi:[1,0,1]
	v_pk_fma_f32 v[84:85], v[100:101], s[16:17], v[84:85] op_sel_hi:[1,0,1]
	v_pk_fma_f32 v[86:87], v[102:103], s[16:17], v[86:87] op_sel_hi:[1,0,1]
	v_pk_fma_f32 v[88:89], v[104:105], s[16:17], v[88:89] op_sel_hi:[1,0,1]
	v_pk_fma_f32 v[90:91], v[106:107], s[16:17], v[90:91] op_sel_hi:[1,0,1]
	v_pk_fma_f32 v[92:93], v[108:109], s[16:17], v[92:93] op_sel_hi:[1,0,1]
	v_pk_fma_f32 v[94:95], v[110:111], s[16:17], v[94:95] op_sel_hi:[1,0,1]
	v_pk_mul_f32 v[116:117], v[80:81], v[80:81]
	v_pk_mul_f32 v[118:119], v[82:83], v[82:83]
	v_pk_mul_f32 v[120:121], v[84:85], v[84:85]
	v_pk_mul_f32 v[122:123], v[86:87], v[86:87]
	v_pk_mul_f32 v[124:125], v[88:89], v[88:89]
	v_pk_mul_f32 v[126:127], v[90:91], v[90:91]
	v_pk_mul_f32 v[128:129], v[92:93], v[92:93]
	v_pk_mul_f32 v[130:131], v[94:95], v[94:95]
	v_add_f32_e32 v112, v116, v117
	v_add_f32_e32 v112, v118, v112
	v_add_f32_e32 v112, v119, v112
	v_add_f32_e32 v112, v120, v112
	v_add_f32_e32 v112, v121, v112
	v_add_f32_e32 v112, v122, v112
	v_add_f32_e32 v112, v123, v112
	v_add_f32_e32 v112, v124, v112
	v_add_f32_e32 v112, v125, v112
	v_add_f32_e32 v112, v126, v112
	v_add_f32_e32 v112, v127, v112
	v_add_f32_e32 v112, v128, v112
	v_add_f32_e32 v112, v129, v112
	v_add_f32_e32 v112, v130, v112
	v_add_f32_e32 v112, v131, v112
	v_cvt_pk_bf16_f32 v132, v80, v81
	v_cvt_pk_bf16_f32 v133, v82, v83
	v_cvt_pk_bf16_f32 v134, v84, v85
	v_cvt_pk_bf16_f32 v135, v86, v87
	v_cvt_pk_bf16_f32 v136, v88, v89
	v_cvt_pk_bf16_f32 v137, v90, v91
	v_cvt_pk_bf16_f32 v138, v92, v93
	v_cvt_pk_bf16_f32 v139, v94, v95
	s_lshl_b32 s3, s0, 11
	s_add_u32 s62, s14, s3
	s_addc_u32 s65, s15, 0
	v_add_f32_dpp v112, v112, v112 quad_perm:[1,0,3,2] row_mask:0xf bank_mask:0xf
	s_mov_b32 s80, s62
	s_mov_b32 s81, s65
	v_add_f32_dpp v112, v112, v112 quad_perm:[2,3,0,1] row_mask:0xf bank_mask:0xf
	s_lshl_b32 s3, s0, 10
	s_add_u32 s82, s30, s3
	v_add_f32_dpp v112, v112, v112 row_half_mirror row_mask:0xf bank_mask:0xf
	s_addc_u32 s83, s31, 0
	s_nop 0
	v_add_f32_dpp v112, v112, v112 row_mirror row_mask:0xf bank_mask:0xf
	s_nop 1
	v_add_f32_dpp v112, v112, v112 row_bcast:15 row_mask:0xa bank_mask:0xf
	s_nop 1
	v_add_f32_dpp v112, v112, v112 row_bcast:31 row_mask:0xc bank_mask:0xf
	global_store_dwordx4 v2, v[132:135], s[80:81] sc1
	global_store_dwordx4 v2, v[136:139], s[80:81] offset:1024 sc1
	v_readlane_b32 s41, v112, 63
	s_nop 3
	v_mov_b32_e32 v114, s41
	v_fmamk_f32 v114, v114, 0x3a800000, v6
	v_rsq_f32_e32 v114, v114
	s_nop 0
	v_mul_f32_e32 v116, v80, v114
	v_mul_f32_e32 v117, v81, v114
	v_mul_f32_e32 v118, v82, v114
	v_mul_f32_e32 v119, v83, v114
	v_mul_f32_e32 v120, v84, v114
	v_mul_f32_e32 v121, v85, v114
	v_mul_f32_e32 v122, v86, v114
	v_mul_f32_e32 v123, v87, v114
	v_mul_f32_e32 v124, v88, v114
	v_mul_f32_e32 v125, v89, v114
	v_mul_f32_e32 v126, v90, v114
	v_mul_f32_e32 v127, v91, v114
	v_mul_f32_e32 v128, v92, v114
	v_mul_f32_e32 v129, v93, v114
	v_mul_f32_e32 v130, v94, v114
	v_mul_f32_e32 v131, v95, v114
	v_cvt_pk_fp8_f32 v140, v116, v117
	v_cvt_pk_fp8_f32 v141, v120, v121
	v_cvt_pk_fp8_f32 v142, v124, v125
	v_cvt_pk_fp8_f32 v143, v128, v129
	v_cvt_pk_fp8_f32 v140, v118, v119 op_sel:[0,0,1]
	v_cvt_pk_fp8_f32 v141, v122, v123 op_sel:[0,0,1]
	v_cvt_pk_fp8_f32 v142, v126, v127 op_sel:[0,0,1]
	v_cvt_pk_fp8_f32 v143, v130, v131 op_sel:[0,0,1]
	s_nop 0
	global_store_dwordx2 v3, v[140:141], s[82:83] sc1
	global_store_dwordx2 v3, v[142:143], s[82:83] offset:512 sc1
	s_mov_b32 s0, s1
	s_cmp_lt_i32 s0, 0x10000
	s_cbranch_scc0 .Lcmb0_done
.Lcmb0_loop:
	s_add_i32 s1, s0, s50
	s_add_i32 s13, s1, s50
	s_min_i32 s3, s13, 0xffff
	s_lshl_b32 s3, s3, 4
	s_add_u32 s36, s6, s3
	s_addc_u32 s37, s7, 0
	global_load_dwordx4 v[16:19], v5, s[36:37]
	s_waitcnt vmcnt(15)
	v_readfirstlane_b32 s56, v12
	v_readfirstlane_b32 s57, v13
	v_readfirstlane_b32 s58, v14
	v_readfirstlane_b32 s59, v15
	s_min_i32 s3, s1, 0xffff
	s_lshl_b32 s3, s3, 11
	s_add_u32 s60, s8, s3
	s_addc_u32 s61, s9, 0
	global_load_dwordx4 v[20:23], v2, s[60:61]
	global_load_dwordx4 v[24:27], v2, s[60:61] offset:1024
	s_lshl_b32 s3, s56, 10
	s_add_u32 s68, s10, s3
	s_addc_u32 s69, s11, 0
	global_load_dwordx2 v[28:29], v3, s[68:69]
	global_load_dwordx2 v[36:37], v3, s[68:69] offset:512
	s_lshl_b32 s3, s57, 10
	s_add_u32 s72, s10, s3
	s_addc_u32 s73, s11, 0
	global_load_dwordx2 v[30:31], v3, s[72:73]
	global_load_dwordx2 v[38:39], v3, s[72:73] offset:512
	s_lshl_b32 s3, s58, 10
	s_add_u32 s74, s10, s3
	s_addc_u32 s75, s11, 0
	global_load_dwordx2 v[32:33], v3, s[74:75]
	global_load_dwordx2 v[40:41], v3, s[74:75] offset:512
	s_lshl_b32 s3, s59, 10
	s_add_u32 s78, s10, s3
	s_addc_u32 s79, s11, 0
	global_load_dwordx2 v[34:35], v3, s[78:79]
	global_load_dwordx2 v[42:43], v3, s[78:79] offset:512
	s_waitcnt vmcnt(15)
	v_lshlrev_b32_e32 v80, 16, v48
	v_and_b32_e32 v81, 0xffff0000, v48
	v_lshlrev_b32_e32 v82, 16, v49
	v_and_b32_e32 v83, 0xffff0000, v49
	v_lshlrev_b32_e32 v84, 16, v50
	v_and_b32_e32 v85, 0xffff0000, v50
	v_lshlrev_b32_e32 v86, 16, v51
	v_and_b32_e32 v87, 0xffff0000, v51
	v_lshlrev_b32_e32 v88, 16, v52
	v_and_b32_e32 v89, 0xffff0000, v52
	v_lshlrev_b32_e32 v90, 16, v53
	v_and_b32_e32 v91, 0xffff0000, v53
	v_lshlrev_b32_e32 v92, 16, v54
	v_and_b32_e32 v93, 0xffff0000, v54
	v_lshlrev_b32_e32 v94, 16, v55
	v_and_b32_e32 v95, 0xffff0000, v55
	v_cvt_pk_f32_fp8_e32 v[96:97], v56
	v_cvt_pk_f32_fp8_sdwa v[98:99], v56 src0_sel:WORD_1
	v_cvt_pk_f32_fp8_e32 v[100:101], v57
	v_cvt_pk_f32_fp8_sdwa v[102:103], v57 src0_sel:WORD_1
	v_cvt_pk_f32_fp8_e32 v[104:105], v64
	v_cvt_pk_f32_fp8_sdwa v[106:107], v64 src0_sel:WORD_1
	v_cvt_pk_f32_fp8_e32 v[108:109], v65
	v_cvt_pk_f32_fp8_sdwa v[110:111], v65 src0_sel:WORD_1
	v_pk_fma_f32 v[80:81], v[96:97], s[16:17], v[80:81] op_sel_hi:[1,0,1]
	v_pk_fma_f32 v[82:83], v[98:99], s[16:17], v[82:83] op_sel_hi:[1,0,1]
	v_pk_fma_f32 v[84:85], v[100:101], s[16:17], v[84:85] op_sel_hi:[1,0,1]
	v_pk_fma_f32 v[86:87], v[102:103], s[16:17], v[86:87] op_sel_hi:[1,0,1]
	v_pk_fma_f32 v[88:89], v[104:105], s[16:17], v[88:89] op_sel_hi:[1,0,1]
	v_pk_fma_f32 v[90:91], v[106:107], s[16:17], v[90:91] op_sel_hi:[1,0,1]
	v_pk_fma_f32 v[92:93], v[108:109], s[16:17], v[92:93] op_sel_hi:[1,0,1]
	v_pk_fma_f32 v[94:95], v[110:111], s[16:17], v[94:95] op_sel_hi:[1,0,1]
	v_cvt_pk_f32_fp8_e32 v[96:97], v58
	v_cvt_pk_f32_fp8_sdwa v[98:99], v58 src0_sel:WORD_1
	v_cvt_pk_f32_fp8_e32 v[100:101], v59
	v_cvt_pk_f32_fp8_sdwa v[102:103], v59 src0_sel:WORD_1
	v_cvt_pk_f32_fp8_e32 v[104:105], v66
	v_cvt_pk_f32_fp8_sdwa v[106:107], v66 src0_sel:WORD_1
	v_cvt_pk_f32_fp8_e32 v[108:109], v67
	v_cvt_pk_f32_fp8_sdwa v[110:111], v67 src0_sel:WORD_1
	v_pk_fma_f32 v[80:81], v[96:97], s[16:17], v[80:81] op_sel_hi:[1,0,1]
	v_pk_fma_f32 v[82:83], v[98:99], s[16:17], v[82:83] op_sel_hi:[1,0,1]
	v_pk_fma_f32 v[84:85], v[100:101], s[16:17], v[84:85] op_sel_hi:[1,0,1]
	v_pk_fma_f32 v[86:87], v[102:103], s[16:17], v[86:87] op_sel_hi:[1,0,1]
	v_pk_fma_f32 v[88:89], v[104:105], s[16:17], v[88:89] op_sel_hi:[1,0,1]
	v_pk_fma_f32 v[90:91], v[106:107], s[16:17], v[90:91] op_sel_hi:[1,0,1]
	v_pk_fma_f32 v[92:93], v[108:109], s[16:17], v[92:93] op_sel_hi:[1,0,1]
	v_pk_fma_f32 v[94:95], v[110:111], s[16:17], v[94:95] op_sel_hi:[1,0,1]
	v_cvt_pk_f32_fp8_e32 v[96:97], v60
	v_cvt_pk_f32_fp8_sdwa v[98:99], v60 src0_sel:WORD_1
	v_cvt_pk_f32_fp8_e32 v[100:101], v61
	v_cvt_pk_f32_fp8_sdwa v[102:103], v61 src0_sel:WORD_1
	v_cvt_pk_f32_fp8_e32 v[104:105], v68
	v_cvt_pk_f32_fp8_sdwa v[106:107], v68 src0_sel:WORD_1
	v_cvt_pk_f32_fp8_e32 v[108:109], v69
	v_cvt_pk_f32_fp8_sdwa v[110:111], v69 src0_sel:WORD_1
	v_pk_fma_f32 v[80:81], v[96:97], s[16:17], v[80:81] op_sel_hi:[1,0,1]
	v_pk_fma_f32 v[82:83], v[98:99], s[16:17], v[82:83] op_sel_hi:[1,0,1]
	v_pk_fma_f32 v[84:85], v[100:101], s[16:17], v[84:85] op_sel_hi:[1,0,1]
	v_pk_fma_f32 v[86:87], v[102:103], s[16:17], v[86:87] op_sel_hi:[1,0,1]
	v_pk_fma_f32 v[88:89], v[104:105], s[16:17], v[88:89] op_sel_hi:[1,0,1]
	v_pk_fma_f32 v[90:91], v[106:107], s[16:17], v[90:91] op_sel_hi:[1,0,1]
	v_pk_fma_f32 v[92:93], v[108:109], s[16:17], v[92:93] op_sel_hi:[1,0,1]
	v_pk_fma_f32 v[94:95], v[110:111], s[16:17], v[94:95] op_sel_hi:[1,0,1]
	v_cvt_pk_f32_fp8_e32 v[96:97], v62
	v_cvt_pk_f32_fp8_sdwa v[98:99], v62 src0_sel:WORD_1
	v_cvt_pk_f32_fp8_e32 v[100:101], v63
	v_cvt_pk_f32_fp8_sdwa v[102:103], v63 src0_sel:WORD_1
	v_cvt_pk_f32_fp8_e32 v[104:105], v70
	v_cvt_pk_f32_fp8_sdwa v[106:107], v70 src0_sel:WORD_1
	v_cvt_pk_f32_fp8_e32 v[108:109], v71
	v_cvt_pk_f32_fp8_sdwa v[110:111], v71 src0_sel:WORD_1
	v_pk_fma_f32 v[80:81], v[96:97], s[16:17], v[80:81] op_sel_hi:[1,0,1]
	v_pk_fma_f32 v[82:83], v[98:99], s[16:17], v[82:83] op_sel_hi:[1,0,1]
	v_pk_fma_f32 v[84:85], v[100:101], s[16:17], v[84:85] op_sel_hi:[1,0,1]
	v_pk_fma_f32 v[86:87], v[102:103], s[16:17], v[86:87] op_sel_hi:[1,0,1]
	v_pk_fma_f32 v[88:89], v[104:105], s[16:17], v[88:89] op_sel_hi:[1,0,1]
	v_pk_fma_f32 v[90:91], v[106:107], s[16:17], v[90:91] op_sel_hi:[1,0,1]
	v_pk_fma_f32 v[92:93], v[108:109], s[16:17], v[92:93] op_sel_hi:[1,0,1]
	v_pk_fma_f32 v[94:95], v[110:111], s[16:17], v[94:95] op_sel_hi:[1,0,1]
	v_pk_mul_f32 v[116:117], v[80:81], v[80:81]
	v_pk_mul_f32 v[118:119], v[82:83], v[82:83]
	v_pk_mul_f32 v[120:121], v[84:85], v[84:85]
	v_pk_mul_f32 v[122:123], v[86:87], v[86:87]
	v_pk_mul_f32 v[124:125], v[88:89], v[88:89]
	v_pk_mul_f32 v[126:127], v[90:91], v[90:91]
	v_pk_mul_f32 v[128:129], v[92:93], v[92:93]
	v_pk_mul_f32 v[130:131], v[94:95], v[94:95]
	v_add_f32_e32 v112, v116, v117
	v_add_f32_e32 v112, v118, v112
	v_add_f32_e32 v112, v119, v112
	v_add_f32_e32 v112, v120, v112
	v_add_f32_e32 v112, v121, v112
	v_add_f32_e32 v112, v122, v112
	v_add_f32_e32 v112, v123, v112
	v_add_f32_e32 v112, v124, v112
	v_add_f32_e32 v112, v125, v112
	v_add_f32_e32 v112, v126, v112
	v_add_f32_e32 v112, v127, v112
	v_add_f32_e32 v112, v128, v112
	v_add_f32_e32 v112, v129, v112
	v_add_f32_e32 v112, v130, v112
	v_add_f32_e32 v112, v131, v112
	v_cvt_pk_bf16_f32 v132, v80, v81
	v_cvt_pk_bf16_f32 v133, v82, v83
	v_cvt_pk_bf16_f32 v134, v84, v85
	v_cvt_pk_bf16_f32 v135, v86, v87
	v_cvt_pk_bf16_f32 v136, v88, v89
	v_cvt_pk_bf16_f32 v137, v90, v91
	v_cvt_pk_bf16_f32 v138, v92, v93
	v_cvt_pk_bf16_f32 v139, v94, v95
	s_lshl_b32 s3, s0, 11
	s_add_u32 s62, s14, s3
	s_addc_u32 s65, s15, 0
	v_add_f32_dpp v112, v112, v112 quad_perm:[1,0,3,2] row_mask:0xf bank_mask:0xf
	s_mov_b32 s80, s62
	s_mov_b32 s81, s65
	v_add_f32_dpp v112, v112, v112 quad_perm:[2,3,0,1] row_mask:0xf bank_mask:0xf
	s_lshl_b32 s3, s0, 10
	s_add_u32 s82, s30, s3
	v_add_f32_dpp v112, v112, v112 row_half_mirror row_mask:0xf bank_mask:0xf
	s_addc_u32 s83, s31, 0
	s_nop 0
	v_add_f32_dpp v112, v112, v112 row_mirror row_mask:0xf bank_mask:0xf
	s_nop 1
	v_add_f32_dpp v112, v112, v112 row_bcast:15 row_mask:0xa bank_mask:0xf
	s_nop 1
	v_add_f32_dpp v112, v112, v112 row_bcast:31 row_mask:0xc bank_mask:0xf
	global_store_dwordx4 v2, v[132:135], s[80:81] sc1
	global_store_dwordx4 v2, v[136:139], s[80:81] offset:1024 sc1
	v_readlane_b32 s41, v112, 63
	s_nop 3
	v_mov_b32_e32 v114, s41
	v_fmamk_f32 v114, v114, 0x3a800000, v6
	v_rsq_f32_e32 v114, v114
	s_nop 0
	v_mul_f32_e32 v116, v80, v114
	v_mul_f32_e32 v117, v81, v114
	v_mul_f32_e32 v118, v82, v114
	v_mul_f32_e32 v119, v83, v114
	v_mul_f32_e32 v120, v84, v114
	v_mul_f32_e32 v121, v85, v114
	v_mul_f32_e32 v122, v86, v114
	v_mul_f32_e32 v123, v87, v114
	v_mul_f32_e32 v124, v88, v114
	v_mul_f32_e32 v125, v89, v114
	v_mul_f32_e32 v126, v90, v114
	v_mul_f32_e32 v127, v91, v114
	v_mul_f32_e32 v128, v92, v114
	v_mul_f32_e32 v129, v93, v114
	v_mul_f32_e32 v130, v94, v114
	v_mul_f32_e32 v131, v95, v114
	v_cvt_pk_fp8_f32 v140, v116, v117
	v_cvt_pk_fp8_f32 v141, v120, v121
	v_cvt_pk_fp8_f32 v142, v124, v125
	v_cvt_pk_fp8_f32 v143, v128, v129
	v_cvt_pk_fp8_f32 v140, v118, v119 op_sel:[0,0,1]
	v_cvt_pk_fp8_f32 v141, v122, v123 op_sel:[0,0,1]
	v_cvt_pk_fp8_f32 v142, v126, v127 op_sel:[0,0,1]
	v_cvt_pk_fp8_f32 v143, v130, v131 op_sel:[0,0,1]
	s_nop 0
	global_store_dwordx2 v3, v[140:141], s[82:83] sc1
	global_store_dwordx2 v3, v[142:143], s[82:83] offset:512 sc1
	s_mov_b32 s0, s1
	s_cmp_lt_i32 s0, 0x10000
	s_cbranch_scc0 .Lcmb0_done
	s_add_i32 s1, s0, s50
	s_add_i32 s13, s1, s50
	s_min_i32 s3, s13, 0xffff
	s_lshl_b32 s3, s3, 4
	s_add_u32 s34, s6, s3
	s_addc_u32 s35, s7, 0
	global_load_dwordx4 v[12:15], v5, s[34:35]
	s_waitcnt vmcnt(15)
	v_readfirstlane_b32 s56, v16
	v_readfirstlane_b32 s57, v17
	v_readfirstlane_b32 s58, v18
	v_readfirstlane_b32 s59, v19
	s_min_i32 s3, s1, 0xffff
	s_lshl_b32 s3, s3, 11
	s_add_u32 s60, s8, s3
	s_addc_u32 s61, s9, 0
	global_load_dwordx4 v[48:51], v2, s[60:61]
	global_load_dwordx4 v[52:55], v2, s[60:61] offset:1024
	s_lshl_b32 s3, s56, 10
	s_add_u32 s68, s10, s3
	s_addc_u32 s69, s11, 0
	global_load_dwordx2 v[56:57], v3, s[68:69]
	global_load_dwordx2 v[64:65], v3, s[68:69] offset:512
	s_lshl_b32 s3, s57, 10
	s_add_u32 s72, s10, s3
	s_addc_u32 s73, s11, 0
	global_load_dwordx2 v[58:59], v3, s[72:73]
	global_load_dwordx2 v[66:67], v3, s[72:73] offset:512
	s_lshl_b32 s3, s58, 10
	s_add_u32 s74, s10, s3
	s_addc_u32 s75, s11, 0
	global_load_dwordx2 v[60:61], v3, s[74:75]
	global_load_dwordx2 v[68:69], v3, s[74:75] offset:512
	s_lshl_b32 s3, s59, 10
	s_add_u32 s78, s10, s3
	s_addc_u32 s79, s11, 0
	global_load_dwordx2 v[62:63], v3, s[78:79]
	global_load_dwordx2 v[70:71], v3, s[78:79] offset:512
	s_waitcnt vmcnt(15)
	v_lshlrev_b32_e32 v80, 16, v20
	v_and_b32_e32 v81, 0xffff0000, v20
	v_lshlrev_b32_e32 v82, 16, v21
	v_and_b32_e32 v83, 0xffff0000, v21
	v_lshlrev_b32_e32 v84, 16, v22
	v_and_b32_e32 v85, 0xffff0000, v22
	v_lshlrev_b32_e32 v86, 16, v23
	v_and_b32_e32 v87, 0xffff0000, v23
	v_lshlrev_b32_e32 v88, 16, v24
	v_and_b32_e32 v89, 0xffff0000, v24
	v_lshlrev_b32_e32 v90, 16, v25
	v_and_b32_e32 v91, 0xffff0000, v25
	v_lshlrev_b32_e32 v92, 16, v26
	v_and_b32_e32 v93, 0xffff0000, v26
	v_lshlrev_b32_e32 v94, 16, v27
	v_and_b32_e32 v95, 0xffff0000, v27
	v_cvt_pk_f32_fp8_e32 v[96:97], v28
	v_cvt_pk_f32_fp8_sdwa v[98:99], v28 src0_sel:WORD_1
	v_cvt_pk_f32_fp8_e32 v[100:101], v29
	v_cvt_pk_f32_fp8_sdwa v[102:103], v29 src0_sel:WORD_1
	v_cvt_pk_f32_fp8_e32 v[104:105], v36
	v_cvt_pk_f32_fp8_sdwa v[106:107], v36 src0_sel:WORD_1
	v_cvt_pk_f32_fp8_e32 v[108:109], v37
	v_cvt_pk_f32_fp8_sdwa v[110:111], v37 src0_sel:WORD_1
	v_pk_fma_f32 v[80:81], v[96:97], s[16:17], v[80:81] op_sel_hi:[1,0,1]
	v_pk_fma_f32 v[82:83], v[98:99], s[16:17], v[82:83] op_sel_hi:[1,0,1]
	v_pk_fma_f32 v[84:85], v[100:101], s[16:17], v[84:85] op_sel_hi:[1,0,1]
	v_pk_fma_f32 v[86:87], v[102:103], s[16:17], v[86:87] op_sel_hi:[1,0,1]
	v_pk_fma_f32 v[88:89], v[104:105], s[16:17], v[88:89] op_sel_hi:[1,0,1]
	v_pk_fma_f32 v[90:91], v[106:107], s[16:17], v[90:91] op_sel_hi:[1,0,1]
	v_pk_fma_f32 v[92:93], v[108:109], s[16:17], v[92:93] op_sel_hi:[1,0,1]
	v_pk_fma_f32 v[94:95], v[110:111], s[16:17], v[94:95] op_sel_hi:[1,0,1]
	v_cvt_pk_f32_fp8_e32 v[96:97], v30
	v_cvt_pk_f32_fp8_sdwa v[98:99], v30 src0_sel:WORD_1
	v_cvt_pk_f32_fp8_e32 v[100:101], v31
	v_cvt_pk_f32_fp8_sdwa v[102:103], v31 src0_sel:WORD_1
	v_cvt_pk_f32_fp8_e32 v[104:105], v38
	v_cvt_pk_f32_fp8_sdwa v[106:107], v38 src0_sel:WORD_1
	v_cvt_pk_f32_fp8_e32 v[108:109], v39
	v_cvt_pk_f32_fp8_sdwa v[110:111], v39 src0_sel:WORD_1
	v_pk_fma_f32 v[80:81], v[96:97], s[16:17], v[80:81] op_sel_hi:[1,0,1]
	v_pk_fma_f32 v[82:83], v[98:99], s[16:17], v[82:83] op_sel_hi:[1,0,1]
	v_pk_fma_f32 v[84:85], v[100:101], s[16:17], v[84:85] op_sel_hi:[1,0,1]
	v_pk_fma_f32 v[86:87], v[102:103], s[16:17], v[86:87] op_sel_hi:[1,0,1]
	v_pk_fma_f32 v[88:89], v[104:105], s[16:17], v[88:89] op_sel_hi:[1,0,1]
	v_pk_fma_f32 v[90:91], v[106:107], s[16:17], v[90:91] op_sel_hi:[1,0,1]
	v_pk_fma_f32 v[92:93], v[108:109], s[16:17], v[92:93] op_sel_hi:[1,0,1]
	v_pk_fma_f32 v[94:95], v[110:111], s[16:17], v[94:95] op_sel_hi:[1,0,1]
	v_cvt_pk_f32_fp8_e32 v[96:97], v32
	v_cvt_pk_f32_fp8_sdwa v[98:99], v32 src0_sel:WORD_1
	v_cvt_pk_f32_fp8_e32 v[100:101], v33
	v_cvt_pk_f32_fp8_sdwa v[102:103], v33 src0_sel:WORD_1
	v_cvt_pk_f32_fp8_e32 v[104:105], v40
	v_cvt_pk_f32_fp8_sdwa v[106:107], v40 src0_sel:WORD_1
	v_cvt_pk_f32_fp8_e32 v[108:109], v41
	v_cvt_pk_f32_fp8_sdwa v[110:111], v41 src0_sel:WORD_1
	v_pk_fma_f32 v[80:81], v[96:97], s[16:17], v[80:81] op_sel_hi:[1,0,1]
	v_pk_fma_f32 v[82:83], v[98:99], s[16:17], v[82:83] op_sel_hi:[1,0,1]
	v_pk_fma_f32 v[84:85], v[100:101], s[16:17], v[84:85] op_sel_hi:[1,0,1]
	v_pk_fma_f32 v[86:87], v[102:103], s[16:17], v[86:87] op_sel_hi:[1,0,1]
	v_pk_fma_f32 v[88:89], v[104:105], s[16:17], v[88:89] op_sel_hi:[1,0,1]
	v_pk_fma_f32 v[90:91], v[106:107], s[16:17], v[90:91] op_sel_hi:[1,0,1]
	v_pk_fma_f32 v[92:93], v[108:109], s[16:17], v[92:93] op_sel_hi:[1,0,1]
	v_pk_fma_f32 v[94:95], v[110:111], s[16:17], v[94:95] op_sel_hi:[1,0,1]
	v_cvt_pk_f32_fp8_e32 v[96:97], v34
	v_cvt_pk_f32_fp8_sdwa v[98:99], v34 src0_sel:WORD_1
	v_cvt_pk_f32_fp8_e32 v[100:101], v35
	v_cvt_pk_f32_fp8_sdwa v[102:103], v35 src0_sel:WORD_1
	v_cvt_pk_f32_fp8_e32 v[104:105], v42
	v_cvt_pk_f32_fp8_sdwa v[106:107], v42 src0_sel:WORD_1
	v_cvt_pk_f32_fp8_e32 v[108:109], v43
	v_cvt_pk_f32_fp8_sdwa v[110:111], v43 src0_sel:WORD_1
	v_pk_fma_f32 v[80:81], v[96:97], s[16:17], v[80:81] op_sel_hi:[1,0,1]
	v_pk_fma_f32 v[82:83], v[98:99], s[16:17], v[82:83] op_sel_hi:[1,0,1]
	v_pk_fma_f32 v[84:85], v[100:101], s[16:17], v[84:85] op_sel_hi:[1,0,1]
	v_pk_fma_f32 v[86:87], v[102:103], s[16:17], v[86:87] op_sel_hi:[1,0,1]
	v_pk_fma_f32 v[88:89], v[104:105], s[16:17], v[88:89] op_sel_hi:[1,0,1]
	v_pk_fma_f32 v[90:91], v[106:107], s[16:17], v[90:91] op_sel_hi:[1,0,1]
	v_pk_fma_f32 v[92:93], v[108:109], s[16:17], v[92:93] op_sel_hi:[1,0,1]
	v_pk_fma_f32 v[94:95], v[110:111], s[16:17], v[94:95] op_sel_hi:[1,0,1]
	v_pk_mul_f32 v[116:117], v[80:81], v[80:81]
	v_pk_mul_f32 v[118:119], v[82:83], v[82:83]
	v_pk_mul_f32 v[120:121], v[84:85], v[84:85]
	v_pk_mul_f32 v[122:123], v[86:87], v[86:87]
	v_pk_mul_f32 v[124:125], v[88:89], v[88:89]
	v_pk_mul_f32 v[126:127], v[90:91], v[90:91]
	v_pk_mul_f32 v[128:129], v[92:93], v[92:93]
	v_pk_mul_f32 v[130:131], v[94:95], v[94:95]
	v_add_f32_e32 v112, v116, v117
	v_add_f32_e32 v112, v118, v112
	v_add_f32_e32 v112, v119, v112
	v_add_f32_e32 v112, v120, v112
	v_add_f32_e32 v112, v121, v112
	v_add_f32_e32 v112, v122, v112
	v_add_f32_e32 v112, v123, v112
	v_add_f32_e32 v112, v124, v112
	v_add_f32_e32 v112, v125, v112
	v_add_f32_e32 v112, v126, v112
	v_add_f32_e32 v112, v127, v112
	v_add_f32_e32 v112, v128, v112
	v_add_f32_e32 v112, v129, v112
	v_add_f32_e32 v112, v130, v112
	v_add_f32_e32 v112, v131, v112
	v_cvt_pk_bf16_f32 v132, v80, v81
	v_cvt_pk_bf16_f32 v133, v82, v83
	v_cvt_pk_bf16_f32 v134, v84, v85
	v_cvt_pk_bf16_f32 v135, v86, v87
	v_cvt_pk_bf16_f32 v136, v88, v89
	v_cvt_pk_bf16_f32 v137, v90, v91
	v_cvt_pk_bf16_f32 v138, v92, v93
	v_cvt_pk_bf16_f32 v139, v94, v95
	s_lshl_b32 s3, s0, 11
	s_add_u32 s62, s14, s3
	s_addc_u32 s65, s15, 0
	v_add_f32_dpp v112, v112, v112 quad_perm:[1,0,3,2] row_mask:0xf bank_mask:0xf
	s_mov_b32 s80, s62
	s_mov_b32 s81, s65
	v_add_f32_dpp v112, v112, v112 quad_perm:[2,3,0,1] row_mask:0xf bank_mask:0xf
	s_lshl_b32 s3, s0, 10
	s_add_u32 s82, s30, s3
	v_add_f32_dpp v112, v112, v112 row_half_mirror row_mask:0xf bank_mask:0xf
	s_addc_u32 s83, s31, 0
	s_nop 0
	v_add_f32_dpp v112, v112, v112 row_mirror row_mask:0xf bank_mask:0xf
	s_nop 1
	v_add_f32_dpp v112, v112, v112 row_bcast:15 row_mask:0xa bank_mask:0xf
	s_nop 1
	v_add_f32_dpp v112, v112, v112 row_bcast:31 row_mask:0xc bank_mask:0xf
	global_store_dwordx4 v2, v[132:135], s[80:81] sc1
	global_store_dwordx4 v2, v[136:139], s[80:81] offset:1024 sc1
	v_readlane_b32 s41, v112, 63
	s_nop 3
	v_mov_b32_e32 v114, s41
	v_fmamk_f32 v114, v114, 0x3a800000, v6
	v_rsq_f32_e32 v114, v114
	s_nop 0
	v_mul_f32_e32 v116, v80, v114
	v_mul_f32_e32 v117, v81, v114
	v_mul_f32_e32 v118, v82, v114
	v_mul_f32_e32 v119, v83, v114
	v_mul_f32_e32 v120, v84, v114
	v_mul_f32_e32 v121, v85, v114
	v_mul_f32_e32 v122, v86, v114
	v_mul_f32_e32 v123, v87, v114
	v_mul_f32_e32 v124, v88, v114
	v_mul_f32_e32 v125, v89, v114
	v_mul_f32_e32 v126, v90, v114
	v_mul_f32_e32 v127, v91, v114
	v_mul_f32_e32 v128, v92, v114
	v_mul_f32_e32 v129, v93, v114
	v_mul_f32_e32 v130, v94, v114
	v_mul_f32_e32 v131, v95, v114
	v_cvt_pk_fp8_f32 v140, v116, v117
	v_cvt_pk_fp8_f32 v141, v120, v121
	v_cvt_pk_fp8_f32 v142, v124, v125
	v_cvt_pk_fp8_f32 v143, v128, v129
	v_cvt_pk_fp8_f32 v140, v118, v119 op_sel:[0,0,1]
	v_cvt_pk_fp8_f32 v141, v122, v123 op_sel:[0,0,1]
	v_cvt_pk_fp8_f32 v142, v126, v127 op_sel:[0,0,1]
	v_cvt_pk_fp8_f32 v143, v130, v131 op_sel:[0,0,1]
	s_nop 0
	global_store_dwordx2 v3, v[140:141], s[82:83] sc1
	global_store_dwordx2 v3, v[142:143], s[82:83] offset:512 sc1
	s_mov_b32 s0, s1
	s_cmp_lt_i32 s0, 0x10000
	s_cbranch_scc0 .Lcmb0_done
	s_branch .Lcmb0_loop

.LBB0_1920:
	v_mul_f32_e32 v2, v27, v27
	v_mul_f32_e32 v3, v21, v21
	v_fmac_f32_e32 v2, v26, v26
	v_fmac_f32_e32 v3, v20, v20
	v_add_f32_e32 v2, v2, v3
	v_mul_f32_e32 v3, v23, v23
	v_mul_f32_e32 v4, v19, v19
	v_fmac_f32_e32 v3, v22, v22
	v_fmac_f32_e32 v4, v18, v18
	v_add_f32_e32 v3, v3, v4
	v_add_f32_e32 v2, v2, v3
	v_mul_f32_e32 v3, v33, v33
	v_mul_f32_e32 v4, v29, v29
	v_fmac_f32_e32 v3, v32, v32
	v_fmac_f32_e32 v4, v28, v28
	v_add_f32_e32 v3, v3, v4
	v_mul_f32_e32 v4, v31, v31
	v_mul_f32_e32 v5, v25, v25
	v_fmac_f32_e32 v4, v30, v30
	v_fmac_f32_e32 v5, v24, v24
	v_add_f32_e32 v4, v4, v5
	v_add_f32_e32 v3, v3, v4
	v_and_b32_e32 v4, 64, v169
	v_add_f32_e32 v2, v2, v3
	v_xor_b32_e32 v3, 16, v169
	v_add_u32_e32 v4, 64, v4
	v_cmp_lt_i32_e32 vcc, v3, v4
	s_nop 1
	v_cndmask_b32_e32 v3, v169, v3, vcc
	v_lshlrev_b32_e32 v3, 2, v3
	ds_bpermute_b32 v3, v3, v2
	s_waitcnt lgkmcnt(0)
	v_add_f32_e32 v2, v2, v3
	v_xor_b32_e32 v3, 32, v169
	v_cmp_lt_i32_e32 vcc, v3, v4
	s_nop 1
	v_cndmask_b32_e32 v3, v169, v3, vcc
	v_lshlrev_b32_e32 v3, 2, v3
	ds_bpermute_b32 v3, v3, v2
	s_waitcnt lgkmcnt(0)
	v_add_f32_e32 v2, v2, v3
	v_max_f32_e32 v3, v172, v172
	v_max_f32_e32 v2, v3, v2
	v_xor_b32_e32 v3, 1, v169
	v_cmp_lt_i32_e32 vcc, v3, v4
	s_nop 1
	v_cndmask_b32_e32 v3, v169, v3, vcc
	v_lshlrev_b32_e32 v3, 2, v3
	ds_bpermute_b32 v3, v3, v2
	s_waitcnt lgkmcnt(0)
	v_max_f32_e32 v3, v3, v3
	v_max_f32_e32 v2, v2, v3
	v_xor_b32_e32 v3, 2, v169
	v_cmp_lt_i32_e32 vcc, v3, v4
	s_nop 1
	v_cndmask_b32_e32 v3, v169, v3, vcc
	v_lshlrev_b32_e32 v3, 2, v3
	ds_bpermute_b32 v3, v3, v2
	s_waitcnt lgkmcnt(0)
	v_max_f32_e32 v3, v3, v3
	v_max_f32_e32 v2, v2, v3
	v_xor_b32_e32 v3, 4, v169
	v_cmp_lt_i32_e32 vcc, v3, v4
	s_nop 1
	v_cndmask_b32_e32 v3, v169, v3, vcc
	v_lshlrev_b32_e32 v3, 2, v3
	ds_bpermute_b32 v3, v3, v2
	s_waitcnt lgkmcnt(0)
	v_max_f32_e32 v3, v3, v3
	v_max_f32_e32 v2, v2, v3
	v_xor_b32_e32 v3, 8, v169
	v_cmp_lt_i32_e32 vcc, v3, v4
	s_nop 1
	v_cndmask_b32_e32 v3, v169, v3, vcc
	v_lshlrev_b32_e32 v3, 2, v3
	ds_bpermute_b32 v3, v3, v2
	v_cmp_eq_u32_e32 vcc, 0, v170
	s_and_saveexec_b64 s[10:11], vcc
	s_cbranch_execz .LBB0_1922
	s_ashr_i32 s19, s18, 31
	s_lshl_b64 s[12:13], s[18:19], 4
	s_or_b32 s12, s12, s51
	s_or_b32 s12, s12, s49
	s_ashr_i32 s77, s76, 31
	s_lshl_b64 s[12:13], s[12:13], 4
	s_add_u32 s14, s53, s12
	v_readlane_b32 s12, v254, 32
	s_addc_u32 s15, s12, s13
	s_lshl_b64 s[12:13], s[82:83], 3
	s_add_u32 s14, s14, s12
	s_addc_u32 s15, s15, s13
	s_lshl_b64 s[12:13], s[76:77], 2
	s_waitcnt lgkmcnt(0)
	v_max_f32_e32 v3, v3, v3
	v_max_f32_e32 v2, v2, v2
	s_add_u32 s12, s14, s12
	v_max_f32_e32 v2, v2, v3
	s_addc_u32 s13, s15, s13
	global_store_dword v155, v2, s[12:13] sc1

.LBB0_1973:
	s_andn2_saveexec_b64 s[12:13], s[12:13]
	s_cbranch_execz .LBB0_1993
	s_mov_b64 s[14:15], exec
	s_waitcnt lgkmcnt(0)
	s_waitcnt vmcnt(0)
	v_mbcnt_lo_u32_b32 v2, s14, 0
	v_mbcnt_hi_u32_b32 v2, s15, v2
	v_cmp_eq_u32_e32 vcc, 0, v2
	s_and_saveexec_b64 s[16:17], vcc
	s_cbranch_execz .LBB0_1976
	s_bcnt1_i32_b64 s0, s[14:15]
	v_mov_b32_e32 v4, s0
	v_readlane_b32 s0, v254, 25
	v_mov_b32_e32 v3, 0x7000
	v_readlane_b32 s1, v254, 26
	s_nop 4
	global_atomic_add v3, v3, v4, s[0:1] offset:1024 sc0

.LBB0_1996:
	s_or_b64 exec, exec, s[50:51]
	v_mul_f32_e32 v5, 0x4f800000, v4
	v_cmp_gt_f32_e32 vcc, s7, v4
	s_mov_b32 s33, 0x42b40000
	v_readlane_b32 s90, v254, 27
	v_cndmask_b32_e32 v4, v4, v5, vcc
	v_sqrt_f32_e32 v5, v4
	v_readlane_b32 s91, v254, 28
	v_add_u32_e32 v16, -1, v5
	v_fma_f32 v19, -v16, v5, v4
	v_add_u32_e32 v18, 1, v5
	v_cmp_ge_f32_e64 s[48:49], 0, v19
	s_nop 1
	v_cndmask_b32_e64 v16, v5, v16, s[48:49]
	v_fma_f32 v5, -v18, v5, v4
	v_cmp_lt_f32_e64 s[48:49], 0, v5
	s_nop 1
	v_cndmask_b32_e64 v5, v16, v18, s[48:49]
	ds_read_b32 v18, v14 offset:1276
	v_mul_f32_e32 v16, 0x37800000, v5
	v_cndmask_b32_e32 v5, v5, v16, vcc
	v_cmp_class_f32_e32 vcc, v4, v32
	s_waitcnt lgkmcnt(0)
	v_sub_f32_e32 v2, v18, v2
	v_cndmask_b32_e32 v4, v5, v4, vcc
	v_mul_f32_e32 v5, v3, v4
	v_cmp_nge_f32_e32 vcc, s33, v5
	v_fma_f32 v3, v3, v4, v2
	s_mov_b32 s33, 0x42c80000
	v_cmp_nge_f32_e64 s[48:49], s33, v3
	v_cmp_le_f32_e64 s[50:51], 0, v2
	s_or_b64 s[48:49], vcc, s[48:49]
	s_mov_b32 s33, 0x7ffffffe
	v_cndmask_b32_e64 v2, 0, v37, s[50:51]
	v_cndmask_b32_e64 v2, v2, 0, s[48:49]
	v_and_or_b32 v4, v17, s33, v2
	v_lshl_add_u32 v2, s86, 5, v1
	v_ashrrev_i32_e32 v3, 31, v2
	v_lshl_add_u64 v[2:3], v[2:3], 2, s[76:77]
	global_store_dword v[2:3], v4, off sc1

.LBB0_2008:
	v_pk_add_f32 v[26:27], v[28:29], v[26:27] op_sel_hi:[0,1]
	v_pk_add_f32 v[4:5], v[28:29], v[4:5] op_sel_hi:[0,1]
	v_pk_mul_f32 v[38:39], v[26:27], s[84:85] op_sel_hi:[1,0]
	v_pk_add_f32 v[24:25], v[28:29], v[24:25] op_sel_hi:[0,1]
	v_pk_add_f32 v[20:21], v[28:29], v[20:21] op_sel_hi:[0,1]
	v_pk_add_f32 v[16:17], v[28:29], v[16:17] op_sel_hi:[0,1]
	v_pk_mul_f32 v[4:5], v[4:5], s[84:85] op_sel_hi:[1,0]
	v_pk_mul_f32 v[40:41], v[24:25], s[84:85] op_sel_hi:[1,0]
	v_pk_mul_f32 v[24:25], v[20:21], s[84:85] op_sel_hi:[1,0]
	v_pk_mul_f32 v[20:21], v[16:17], s[84:85] op_sel_hi:[1,0]
	v_sub_f32_e32 v16, v38, v5
	v_cmp_gt_f32_e32 vcc, s6, v16
	v_pk_add_f32 v[22:23], v[28:29], v[22:23] op_sel_hi:[0,1]
	s_ashr_i32 s87, s86, 31
	v_cndmask_b32_e32 v17, 0, v34, vcc
	v_add_f32_e32 v16, v16, v17
	v_exp_f32_e32 v16, v16
	v_cndmask_b32_e32 v17, 0, v35, vcc
	v_pk_mul_f32 v[22:23], v[22:23], s[84:85] op_sel_hi:[1,0]
	s_lshl_b64 s[58:59], s[86:87], 15
	v_ldexp_f32 v16, v16, v17
	v_sub_f32_e32 v17, v39, v5
	v_cmp_gt_f32_e32 vcc, s6, v17
	v_lshl_add_u64 v[42:43], v[8:9], 0, s[58:59]
	global_store_dwordx4 v[42:43], v[22:25], off offset:16 sc1
	v_cndmask_b32_e32 v26, 0, v34, vcc
	v_add_f32_e32 v17, v17, v26
	v_exp_f32_e32 v17, v17
	v_cndmask_b32_e32 v26, 0, v35, vcc
	ds_write_b128 v10, v[22:25] offset:272
	v_pk_add_f32 v[18:19], v[28:29], v[18:19] op_sel_hi:[0,1]
	v_ldexp_f32 v17, v17, v26
	v_add_f32_e32 v16, v16, v17
	v_sub_f32_e32 v17, v40, v5
	v_cmp_gt_f32_e32 vcc, s6, v17
	v_pk_mul_f32 v[18:19], v[18:19], s[84:85] op_sel_hi:[1,0]
	global_store_dwordx4 v[42:43], v[18:21], off offset:32 sc1
	v_cndmask_b32_e32 v26, 0, v34, vcc
	v_add_f32_e32 v17, v17, v26
	v_exp_f32_e32 v17, v17
	v_cndmask_b32_e32 v26, 0, v35, vcc
	ds_write_b128 v10, v[18:21] offset:288
	v_pk_add_f32 v[2:3], v[28:29], v[2:3] op_sel_hi:[0,1]
	v_ldexp_f32 v17, v17, v26
	v_add_f32_e32 v16, v16, v17
	v_sub_f32_e32 v17, v41, v5
	v_cmp_gt_f32_e32 vcc, s6, v17
	v_pk_mul_f32 v[2:3], v[2:3], s[84:85] op_sel_hi:[1,0]
	global_store_dwordx4 v[42:43], v[2:5], off offset:48 sc1
	v_cndmask_b32_e32 v26, 0, v34, vcc
	v_add_f32_e32 v17, v17, v26
	v_exp_f32_e32 v17, v17
	v_cndmask_b32_e32 v26, 0, v35, vcc
	ds_write_b128 v10, v[2:5] offset:304
	v_sub_f32_e32 v2, v2, v5
	v_ldexp_f32 v17, v17, v26
	v_add_f32_e32 v16, v16, v17
	v_sub_f32_e32 v17, v22, v5
	v_cmp_gt_f32_e32 vcc, s6, v17
	v_sub_f32_e32 v3, v3, v5
	global_store_dwordx4 v[42:43], v[38:41], off sc1
	v_cndmask_b32_e32 v22, 0, v34, vcc
	v_add_f32_e32 v17, v17, v22
	v_exp_f32_e32 v17, v17
	v_cndmask_b32_e32 v22, 0, v35, vcc
	ds_write_b128 v10, v[38:41] offset:256
	v_ldexp_f32 v17, v17, v22
	v_add_f32_e32 v16, v16, v17
	v_sub_f32_e32 v17, v23, v5
	v_cmp_gt_f32_e32 vcc, s6, v17
	s_nop 1
	v_cndmask_b32_e32 v22, 0, v34, vcc
	v_add_f32_e32 v17, v17, v22
	v_exp_f32_e32 v17, v17
	v_cndmask_b32_e32 v22, 0, v35, vcc
	v_ldexp_f32 v17, v17, v22
	v_add_f32_e32 v16, v16, v17
	v_sub_f32_e32 v17, v24, v5
	v_cmp_gt_f32_e32 vcc, s6, v17
	s_nop 1
	v_cndmask_b32_e32 v22, 0, v34, vcc
	v_add_f32_e32 v17, v17, v22
	v_exp_f32_e32 v17, v17
	v_cndmask_b32_e32 v22, 0, v35, vcc
	v_ldexp_f32 v17, v17, v22
	v_add_f32_e32 v16, v16, v17
	v_sub_f32_e32 v17, v25, v5
	v_cmp_gt_f32_e32 vcc, s6, v17
	s_nop 1
	v_cndmask_b32_e32 v22, 0, v34, vcc
	v_add_f32_e32 v17, v17, v22
	v_exp_f32_e32 v17, v17
	v_cndmask_b32_e32 v22, 0, v35, vcc
	v_ldexp_f32 v17, v17, v22
	v_add_f32_e32 v16, v16, v17
	v_sub_f32_e32 v17, v18, v5
	v_cmp_gt_f32_e32 vcc, s6, v17
	s_nop 1
	v_cndmask_b32_e32 v18, 0, v34, vcc
	v_add_f32_e32 v17, v17, v18
	v_exp_f32_e32 v17, v17
	v_cndmask_b32_e32 v18, 0, v35, vcc
	v_ldexp_f32 v17, v17, v18
	v_add_f32_e32 v16, v16, v17
	v_sub_f32_e32 v17, v19, v5
	v_cmp_gt_f32_e32 vcc, s6, v17
	s_nop 1
	v_cndmask_b32_e32 v18, 0, v34, vcc
	v_add_f32_e32 v17, v17, v18
	v_exp_f32_e32 v17, v17
	v_cndmask_b32_e32 v18, 0, v35, vcc
	v_ldexp_f32 v17, v17, v18
	v_add_f32_e32 v16, v16, v17
	v_sub_f32_e32 v17, v20, v5
	v_cmp_gt_f32_e32 vcc, s6, v17
	s_nop 1
	v_cndmask_b32_e32 v18, 0, v34, vcc
	v_add_f32_e32 v17, v17, v18
	v_exp_f32_e32 v17, v17
	v_cndmask_b32_e32 v18, 0, v35, vcc
	v_ldexp_f32 v17, v17, v18
	v_add_f32_e32 v16, v16, v17
	v_sub_f32_e32 v17, v21, v5
	v_cmp_gt_f32_e32 vcc, s6, v17
	s_nop 1
	v_cndmask_b32_e32 v18, 0, v34, vcc
	v_add_f32_e32 v17, v17, v18
	v_exp_f32_e32 v17, v17
	v_cndmask_b32_e32 v18, 0, v35, vcc
	v_cmp_gt_f32_e32 vcc, s6, v2
	v_ldexp_f32 v17, v17, v18
	v_add_f32_e32 v16, v16, v17
	v_cndmask_b32_e32 v17, 0, v34, vcc
	v_add_f32_e32 v2, v2, v17
	v_exp_f32_e32 v2, v2
	v_cndmask_b32_e32 v17, 0, v35, vcc
	v_cmp_gt_f32_e32 vcc, s6, v3
	v_ldexp_f32 v2, v2, v17
	v_add_f32_e32 v2, v16, v2
	v_cndmask_b32_e32 v16, 0, v34, vcc
	v_add_f32_e32 v3, v3, v16
	v_exp_f32_e32 v3, v3
	v_cndmask_b32_e32 v16, 0, v35, vcc
	v_ldexp_f32 v3, v3, v16
	v_add_f32_e32 v2, v2, v3
	v_sub_f32_e32 v3, v4, v5
	v_cmp_gt_f32_e32 vcc, s6, v3
	ds_bpermute_b32 v16, v11, v5
	s_nop 0
	v_cndmask_b32_e32 v4, 0, v34, vcc
	v_add_f32_e32 v3, v3, v4
	v_exp_f32_e32 v3, v3
	v_cndmask_b32_e32 v4, 0, v35, vcc
	v_ldexp_f32 v3, v3, v4
	v_add_f32_e32 v2, v2, v3
	v_sub_f32_e32 v3, v5, v5
	v_cmp_gt_f32_e32 vcc, s6, v3
	s_nop 1
	v_cndmask_b32_e32 v4, 0, v34, vcc
	v_add_f32_e32 v3, v3, v4
	v_exp_f32_e32 v3, v3
	v_cndmask_b32_e32 v4, 0, v35, vcc
	v_ldexp_f32 v3, v3, v4
	v_add_f32_e32 v2, v2, v3
	ds_bpermute_b32 v3, v11, v2
	v_mov_b32_e32 v4, v5
	s_and_saveexec_b64 s[88:89], s[14:15]
	s_cbranch_execz .LBB0_2010
	s_waitcnt lgkmcnt(1)
	v_max_f32_e32 v4, v16, v16
	v_max_f32_e32 v17, v5, v5
	v_max_f32_e32 v4, v17, v4
	v_sub_f32_e32 v5, v5, v4
	v_cmp_gt_f32_e32 vcc, s6, v5
	s_nop 1
	v_cndmask_b32_e32 v17, 0, v34, vcc
	v_add_f32_e32 v5, v5, v17
	v_exp_f32_e32 v5, v5
	v_cndmask_b32_e32 v17, 0, v35, vcc
	v_ldexp_f32 v18, v5, v17
	v_sub_f32_e32 v5, v16, v4
	v_cmp_gt_f32_e32 vcc, s6, v5
	s_nop 1
	v_cndmask_b32_e32 v16, 0, v34, vcc
	v_add_f32_e32 v5, v5, v16
	v_exp_f32_e32 v5, v5
	v_cndmask_b32_e32 v16, 0, v35, vcc
	v_ldexp_f32 v19, v5, v16
	s_waitcnt lgkmcnt(0)
	v_mul_f32_e32 v16, v3, v19
	v_pk_fma_f32 v[2:3], v[2:3], v[18:19], v[16:17] op_sel_hi:[1,1,0]
	v_mov_b32_e32 v5, v4

.LBB0_2069:
	s_andn2_saveexec_b64 s[0:1], s[12:13]
	s_cbranch_execz .LBB0_2089
	s_mov_b64 s[12:13], exec
	s_waitcnt lgkmcnt(0)
	s_waitcnt vmcnt(0)
	v_mbcnt_lo_u32_b32 v2, s12, 0
	v_mbcnt_hi_u32_b32 v2, s13, v2
	v_cmp_eq_u32_e32 vcc, 0, v2
	s_and_saveexec_b64 s[14:15], vcc
	s_cbranch_execz .LBB0_2072
	s_bcnt1_i32_b64 s0, s[12:13]
	v_mov_b32_e32 v3, 0x7000
	v_mov_b32_e32 v4, s0
	global_atomic_add v3, v3, v4, s[52:53] offset:1024 sc0

.LBB0_2379:
	s_lshl_b32 s25, s30, 8
	s_ashr_i32 s30, s23, 2
	s_andn2_b32 s30, s30, 63
	v_and_b32_e32 v104, 63, v82
	s_add_i32 s30, s30, s25
	v_or_b32_e32 v66, s30, v104
	v_ashrrev_i32_e32 v67, 31, v66
	v_lshl_add_u64 v[66:67], v[66:67], 2, s[16:17]
	v_add_co_u32_e32 v68, vcc, s50, v66
	s_lshr_b32 s23, s23, 6
	s_nop 0
	v_addc_co_u32_e32 v69, vcc, 0, v67, vcc
	v_add_co_u32_e32 v70, vcc, s51, v66
	s_mulk_i32 s23, 0xb00
	s_nop 0
	v_addc_co_u32_e32 v71, vcc, 0, v67, vcc
	v_add_co_u32_e32 v72, vcc, s54, v66
	s_add_i32 s23, s23, 0
	s_nop 0
	v_addc_co_u32_e32 v73, vcc, 0, v67, vcc
	v_add_co_u32_e32 v92, vcc, s55, v66
	s_add_i32 s23, s23, 0x20000
	s_nop 0
	v_addc_co_u32_e32 v93, vcc, 0, v67, vcc
	v_add_co_u32_e32 v94, vcc, s56, v66
	s_add_i32 s34, s30, 0x80
	s_nop 0
	v_addc_co_u32_e32 v95, vcc, 0, v67, vcc
	v_add_co_u32_e32 v100, vcc, s57, v66
	s_ashr_i32 s31, s30, 31
	s_nop 0
	v_addc_co_u32_e32 v101, vcc, 0, v67, vcc
	v_add_co_u32_e32 v102, vcc, s58, v66
	s_lshl_b64 s[36:37], s[30:31], 7
	s_nop 0
	v_addc_co_u32_e32 v103, vcc, 0, v67, vcc
	global_load_dword v105, v[66:67], off
	global_load_dword v106, v[68:69], off
	global_load_dword v107, v[70:71], off
	global_load_dword v108, v[72:73], off
	global_load_dword v109, v[92:93], off
	global_load_dword v110, v[94:95], off
	global_load_dword v111, v[100:101], off
	global_load_dword v112, v[102:103], off
	v_add_co_u32_e32 v68, vcc, s59, v66
	s_add_u32 s36, s43, s36
	s_nop 0
	v_addc_co_u32_e32 v69, vcc, 0, v67, vcc
	v_add_co_u32_e32 v70, vcc, s60, v66
	s_addc_u32 s37, s44, s37
	s_nop 0
	v_addc_co_u32_e32 v71, vcc, 0, v67, vcc
	v_add_co_u32_e32 v72, vcc, s61, v66
	s_or_b32 s38, s30, 16
	s_nop 0
	v_addc_co_u32_e32 v73, vcc, 0, v67, vcc
	v_add_co_u32_e32 v92, vcc, s62, v66
	s_ashr_i32 s39, s38, 31
	s_nop 0
	v_addc_co_u32_e32 v93, vcc, 0, v67, vcc
	v_add_co_u32_e32 v94, vcc, s63, v66
	s_nop 1
	v_addc_co_u32_e32 v95, vcc, 0, v67, vcc
	v_add_co_u32_e32 v100, vcc, s64, v66
	s_nop 1
	v_addc_co_u32_e32 v101, vcc, 0, v67, vcc
	v_add_co_u32_e32 v102, vcc, s65, v66
	s_nop 1
	v_addc_co_u32_e32 v103, vcc, 0, v67, vcc
	v_add_co_u32_e32 v66, vcc, s66, v66
	s_nop 1
	v_addc_co_u32_e32 v67, vcc, 0, v67, vcc
	global_load_dword v68, v[68:69], off
	s_nop 0
	global_load_dword v69, v[70:71], off
	s_nop 0
	global_load_dword v70, v[72:73], off
	global_load_dword v71, v[92:93], off
	s_nop 0
	global_load_dword v72, v[94:95], off
	global_load_dword v73, v[100:101], off
	global_load_dword v92, v[102:103], off
	s_nop 0
	global_load_dword v66, v[66:67], off
	s_waitcnt vmcnt(0)
	v_add_f32_e32 v67, v105, v106
	v_lshl_add_u32 v105, v104, 2, s23
	v_add_f32_e32 v93, v107, v108
	v_add_f32_e32 v67, v67, v93
	v_add_f32_e32 v93, v109, v110
	v_add_f32_e32 v94, v111, v112
	v_add_f32_e32 v93, v93, v94
	v_add_f32_e32 v67, v67, v93
	v_add_f32_e32 v68, v68, v69
	v_add_f32_e32 v69, v70, v71
	v_add_f32_e32 v68, v68, v69
	v_add_f32_e32 v69, v72, v73
	v_add_f32_e32 v66, v92, v66
	v_add_f32_e32 v66, v69, v66
	v_add_f32_e32 v66, v68, v66
	v_add_f32_e32 v66, v67, v66
	v_fmamk_f32 v66, v66, 0x3a800000, v99
	v_rsq_f32_e32 v66, v66
	ds_write_b32 v105, v66 offset:2304
	v_or_b32_e32 v66, s34, v104
	v_ashrrev_i32_e32 v67, 31, v66
	v_lshl_add_u64 v[66:67], v[66:67], 2, s[16:17]
	v_add_co_u32_e32 v68, vcc, s50, v66
	s_nop 1
	v_addc_co_u32_e32 v69, vcc, 0, v67, vcc
	v_add_co_u32_e32 v70, vcc, s51, v66
	s_nop 1
	v_addc_co_u32_e32 v71, vcc, 0, v67, vcc
	v_add_co_u32_e32 v72, vcc, s54, v66
	s_nop 1
	v_addc_co_u32_e32 v73, vcc, 0, v67, vcc
	v_add_co_u32_e32 v92, vcc, s55, v66
	s_nop 1
	v_addc_co_u32_e32 v93, vcc, 0, v67, vcc
	v_add_co_u32_e32 v94, vcc, s56, v66
	s_nop 1
	v_addc_co_u32_e32 v95, vcc, 0, v67, vcc
	v_add_co_u32_e32 v100, vcc, s57, v66
	s_nop 1
	v_addc_co_u32_e32 v101, vcc, 0, v67, vcc
	v_add_co_u32_e32 v102, vcc, s58, v66
	s_nop 1
	v_addc_co_u32_e32 v103, vcc, 0, v67, vcc
	global_load_dword v104, v[66:67], off
	global_load_dword v106, v[68:69], off
	global_load_dword v107, v[70:71], off
	global_load_dword v108, v[72:73], off
	global_load_dword v109, v[92:93], off
	global_load_dword v110, v[94:95], off
	global_load_dword v111, v[100:101], off
	global_load_dword v112, v[102:103], off
	v_add_co_u32_e32 v68, vcc, s59, v66
	s_nop 1
	v_addc_co_u32_e32 v69, vcc, 0, v67, vcc
	v_add_co_u32_e32 v70, vcc, s60, v66
	s_nop 1
	v_addc_co_u32_e32 v71, vcc, 0, v67, vcc
	v_add_co_u32_e32 v72, vcc, s61, v66
	s_nop 1
	v_addc_co_u32_e32 v73, vcc, 0, v67, vcc
	v_add_co_u32_e32 v92, vcc, s62, v66
	s_nop 1
	v_addc_co_u32_e32 v93, vcc, 0, v67, vcc
	v_add_co_u32_e32 v94, vcc, s63, v66
	s_nop 1
	v_addc_co_u32_e32 v95, vcc, 0, v67, vcc
	v_add_co_u32_e32 v100, vcc, s64, v66
	s_nop 1
	v_addc_co_u32_e32 v101, vcc, 0, v67, vcc
	v_add_co_u32_e32 v102, vcc, s65, v66
	s_nop 1
	v_addc_co_u32_e32 v103, vcc, 0, v67, vcc
	v_add_co_u32_e32 v66, vcc, s66, v66
	s_nop 1
	v_addc_co_u32_e32 v67, vcc, 0, v67, vcc
	global_load_dword v68, v[68:69], off
	s_nop 0
	global_load_dword v69, v[70:71], off
	s_nop 0
	global_load_dword v70, v[72:73], off
	global_load_dword v71, v[92:93], off
	s_nop 0
	global_load_dword v72, v[94:95], off
	global_load_dword v73, v[100:101], off
	global_load_dword v92, v[102:103], off
	s_nop 0
	global_load_dword v66, v[66:67], off
	v_and_b32_e32 v101, 15, v82
	v_mov_b32_e32 v103, s23
	v_mov_b32_e32 v95, v83
	s_waitcnt vmcnt(14)
	v_add_f32_e32 v67, v104, v106
	s_waitcnt vmcnt(12)
	v_add_f32_e32 v93, v107, v108
	v_add_f32_e32 v67, v67, v93
	s_waitcnt vmcnt(10)
	v_add_f32_e32 v93, v109, v110
	v_lshl_add_u32 v108, v101, 2, s23
	s_waitcnt vmcnt(8)
	v_add_f32_e32 v94, v111, v112
	v_add_f32_e32 v93, v93, v94
	v_add_f32_e32 v67, v67, v93
	v_bfe_u32 v94, v82, 3, 3
	v_mul_u32_u24_e32 v102, 0x90, v94
	v_mov_b32_e32 v93, v83
	s_waitcnt vmcnt(6)
	v_add_f32_e32 v68, v68, v69
	s_waitcnt vmcnt(4)
	v_add_f32_e32 v69, v70, v71
	v_add_f32_e32 v68, v68, v69
	s_waitcnt vmcnt(2)
	v_add_f32_e32 v69, v72, v73
	s_waitcnt vmcnt(0)
	v_add_f32_e32 v66, v92, v66
	v_add_f32_e32 v66, v69, v66
	v_add_f32_e32 v66, v68, v66
	v_add_f32_e32 v66, v67, v66
	v_fmamk_f32 v66, v66, 0x3a800000, v99
	v_rsq_f32_e32 v66, v66
	ds_write_b32 v105, v66 offset:2560
	v_lshlrev_b32_e32 v66, 1, v82
	v_and_b32_e32 v100, 0x60, v66
	global_load_dwordx4 v[70:73], v100, s[12:13] offset:128
	global_load_dwordx4 v[66:69], v100, s[12:13] offset:144
	ds_read_b32 v108, v108 offset:2304
	v_lshlrev_b32_e32 v82, 4, v82
	v_and_b32_e32 v92, 0x70, v82
	v_add3_u32 v109, s23, v102, v92
	v_mad_u32_u24 v102, v101, s67, v103
	v_add_u32_e32 v114, v102, v100
	v_mad_i32_i24 v115, v101, s68, v102
	v_lshlrev_b32_e32 v82, 7, v94
	v_or_b32_e32 v94, 0x400, v82
	v_lshl_add_u64 v[100:101], s[36:37], 0, v[82:83]
	v_lshl_add_u64 v[102:103], s[36:37], 0, v[94:95]
	v_lshl_add_u64 v[100:101], v[100:101], 0, v[92:93]
	v_lshl_add_u64 v[102:103], v[102:103], 0, v[92:93]
	s_lshl_b64 s[36:37], s[38:39], 7
	s_add_u32 s36, s43, s36
	s_addc_u32 s37, s44, s37
	s_or_b32 s38, s30, 32
	s_ashr_i32 s39, s38, 31
	v_lshl_add_u64 v[104:105], s[36:37], 0, v[82:83]
	v_lshl_add_u64 v[106:107], s[36:37], 0, v[94:95]
	s_lshl_b64 s[36:37], s[38:39], 7
	s_add_u32 s36, s43, s36
	s_addc_u32 s37, s44, s37
	s_or_b32 s38, s30, 48
	v_lshl_add_u64 v[104:105], v[104:105], 0, v[92:93]
	v_lshl_add_u64 v[110:111], s[36:37], 0, v[82:83]
	v_lshl_add_u64 v[112:113], s[36:37], 0, v[94:95]
	s_ashr_i32 s39, s38, 31
	v_lshl_add_u64 v[106:107], v[106:107], 0, v[92:93]
	v_lshl_add_u64 v[110:111], v[110:111], 0, v[92:93]
	v_lshl_add_u64 v[112:113], v[112:113], 0, v[92:93]
	s_lshl_b64 s[36:37], s[38:39], 7
	s_add_u32 s36, s43, s36
	s_addc_u32 s37, s44, s37
	s_ashr_i32 s35, s34, 31
	s_lshl_b64 s[34:35], s[34:35], 7
	s_add_u32 s34, s43, s34
	s_addc_u32 s35, s44, s35
	s_waitcnt vmcnt(1) lgkmcnt(0)
	v_pk_fma_f32 v[64:65], v[64:65], v[108:109], v[72:73] op_sel_hi:[1,0,1]
	v_pk_fma_f32 v[62:63], v[62:63], v[108:109], v[70:71] op_sel_hi:[1,0,1]
	s_waitcnt vmcnt(0)
	v_pk_fma_f32 v[60:61], v[60:61], v[108:109], v[68:69] op_sel_hi:[1,0,1]
	v_pk_fma_f32 v[58:59], v[58:59], v[108:109], v[66:67] op_sel_hi:[1,0,1]
	ds_write_b128 v114, v[62:65]
	ds_write_b128 v114, v[58:61] offset:16
	ds_read_b32 v108, v115 offset:2368
	ds_read_b128 v[58:61], v109
	ds_read_b128 v[62:65], v109 offset:1152
	s_waitcnt lgkmcnt(2)
	v_pk_fma_f32 v[56:57], v[56:57], v[108:109], v[72:73] op_sel_hi:[1,0,1]
	v_pk_fma_f32 v[54:55], v[54:55], v[108:109], v[70:71] op_sel_hi:[1,0,1]
	v_pk_fma_f32 v[52:53], v[52:53], v[108:109], v[68:69] op_sel_hi:[1,0,1]
	v_pk_fma_f32 v[50:51], v[50:51], v[108:109], v[66:67] op_sel_hi:[1,0,1]
	ds_write_b128 v114, v[54:57]
	ds_write_b128 v114, v[50:53] offset:16
	ds_read_b32 v108, v115 offset:2432
	s_waitcnt lgkmcnt(4)
	global_store_dwordx4 v[100:101], v[58:61], off sc1
	s_waitcnt lgkmcnt(3)
	global_store_dwordx4 v[102:103], v[62:65], off sc1
	ds_read_b128 v[50:53], v109
	ds_read_b128 v[54:57], v109 offset:1152
	s_waitcnt lgkmcnt(2)
	v_pk_fma_f32 v[48:49], v[48:49], v[108:109], v[72:73] op_sel_hi:[1,0,1]
	v_pk_fma_f32 v[46:47], v[46:47], v[108:109], v[70:71] op_sel_hi:[1,0,1]
	v_pk_fma_f32 v[44:45], v[44:45], v[108:109], v[68:69] op_sel_hi:[1,0,1]
	v_pk_fma_f32 v[42:43], v[42:43], v[108:109], v[66:67] op_sel_hi:[1,0,1]
	ds_write_b128 v114, v[46:49]
	ds_write_b128 v114, v[42:45] offset:16
	ds_read_b128 v[42:45], v109
	ds_read_b128 v[46:49], v109 offset:1152
	ds_read_b32 v58, v115 offset:2496
	s_waitcnt lgkmcnt(6)
	global_store_dwordx4 v[104:105], v[50:53], off sc1
	s_waitcnt lgkmcnt(5)
	global_store_dwordx4 v[106:107], v[54:57], off sc1
	s_waitcnt lgkmcnt(2)
	global_store_dwordx4 v[110:111], v[42:45], off sc1
	s_waitcnt lgkmcnt(1)
	global_store_dwordx4 v[112:113], v[46:49], off sc1
	s_waitcnt lgkmcnt(0)
	v_pk_fma_f32 v[40:41], v[40:41], v[58:59], v[72:73] op_sel_hi:[1,0,1]
	v_pk_fma_f32 v[38:39], v[38:39], v[58:59], v[70:71] op_sel_hi:[1,0,1]
	v_pk_fma_f32 v[36:37], v[36:37], v[58:59], v[68:69] op_sel_hi:[1,0,1]
	v_pk_fma_f32 v[34:35], v[34:35], v[58:59], v[66:67] op_sel_hi:[1,0,1]
	ds_write_b128 v114, v[38:41]
	ds_write_b128 v114, v[34:37] offset:16
	ds_read_b128 v[34:37], v109
	ds_read_b128 v[38:41], v109 offset:1152
	ds_read_b32 v44, v115 offset:2560
	v_lshl_add_u64 v[42:43], s[36:37], 0, v[82:83]
	v_lshl_add_u64 v[42:43], v[42:43], 0, v[92:93]
	s_waitcnt lgkmcnt(2)
	global_store_dwordx4 v[42:43], v[34:37], off sc1
	s_waitcnt lgkmcnt(0)
	v_pk_fma_f32 v[32:33], v[32:33], v[44:45], v[72:73] op_sel_hi:[1,0,1]
	v_lshl_add_u64 v[34:35], s[36:37], 0, v[94:95]
	v_lshl_add_u64 v[34:35], v[34:35], 0, v[92:93]
	v_pk_fma_f32 v[30:31], v[30:31], v[44:45], v[70:71] op_sel_hi:[1,0,1]
	global_store_dwordx4 v[34:35], v[38:41], off sc1
	v_pk_fma_f32 v[28:29], v[28:29], v[44:45], v[68:69] op_sel_hi:[1,0,1]
	v_pk_fma_f32 v[26:27], v[26:27], v[44:45], v[66:67] op_sel_hi:[1,0,1]
	ds_write_b128 v114, v[30:33]
	ds_write_b128 v114, v[26:29] offset:16
	ds_read_b128 v[26:29], v109
	ds_read_b128 v[30:33], v109 offset:1152
	ds_read_b32 v36, v115 offset:2624
	v_lshl_add_u64 v[34:35], s[34:35], 0, v[82:83]
	v_lshl_add_u64 v[34:35], v[34:35], 0, v[92:93]
	s_waitcnt lgkmcnt(2)
	global_store_dwordx4 v[34:35], v[26:29], off sc1
	s_waitcnt lgkmcnt(0)
	v_pk_fma_f32 v[24:25], v[24:25], v[36:37], v[72:73] op_sel_hi:[1,0,1]
	v_lshl_add_u64 v[26:27], s[34:35], 0, v[94:95]
	s_add_i32 s34, s30, 0x90
	v_lshl_add_u64 v[26:27], v[26:27], 0, v[92:93]
	v_pk_fma_f32 v[22:23], v[22:23], v[36:37], v[70:71] op_sel_hi:[1,0,1]
	s_ashr_i32 s35, s34, 31
	global_store_dwordx4 v[26:27], v[30:33], off sc1
	v_pk_fma_f32 v[20:21], v[20:21], v[36:37], v[68:69] op_sel_hi:[1,0,1]
	v_pk_fma_f32 v[18:19], v[18:19], v[36:37], v[66:67] op_sel_hi:[1,0,1]
	s_lshl_b64 s[34:35], s[34:35], 7
	ds_write_b128 v114, v[22:25]
	ds_write_b128 v114, v[18:21] offset:16
	s_add_u32 s34, s43, s34
	ds_read_b128 v[18:21], v109
	ds_read_b128 v[22:25], v109 offset:1152
	ds_read_b32 v28, v115 offset:2688
	s_addc_u32 s35, s44, s35
	v_lshl_add_u64 v[26:27], s[34:35], 0, v[82:83]
	v_lshl_add_u64 v[26:27], v[26:27], 0, v[92:93]
	s_waitcnt lgkmcnt(2)
	global_store_dwordx4 v[26:27], v[18:21], off sc1
	s_waitcnt lgkmcnt(0)
	v_pk_fma_f32 v[16:17], v[16:17], v[28:29], v[72:73] op_sel_hi:[1,0,1]
	v_pk_fma_f32 v[14:15], v[14:15], v[28:29], v[70:71] op_sel_hi:[1,0,1]
	v_lshl_add_u64 v[18:19], s[34:35], 0, v[94:95]
	s_add_i32 s34, s30, 0xa0
	v_lshl_add_u64 v[18:19], v[18:19], 0, v[92:93]
	s_ashr_i32 s35, s34, 31
	global_store_dwordx4 v[18:19], v[22:25], off sc1
	v_pk_fma_f32 v[12:13], v[12:13], v[28:29], v[68:69] op_sel_hi:[1,0,1]
	v_pk_fma_f32 v[10:11], v[10:11], v[28:29], v[66:67] op_sel_hi:[1,0,1]
	s_lshl_b64 s[34:35], s[34:35], 7
	ds_write_b128 v114, v[14:17]
	ds_write_b128 v114, v[10:13] offset:16
	s_add_u32 s34, s43, s34
	ds_read_b128 v[10:13], v109
	ds_read_b128 v[14:17], v109 offset:1152
	ds_read_b32 v20, v115 offset:2752
	s_addc_u32 s35, s44, s35
	v_lshl_add_u64 v[18:19], s[34:35], 0, v[82:83]
	v_lshl_add_u64 v[18:19], v[18:19], 0, v[92:93]
	s_waitcnt lgkmcnt(2)
	global_store_dwordx4 v[18:19], v[10:13], off sc1
	s_waitcnt lgkmcnt(0)
	v_pk_fma_f32 v[8:9], v[8:9], v[20:21], v[72:73] op_sel_hi:[1,0,1]
	v_pk_fma_f32 v[6:7], v[6:7], v[20:21], v[70:71] op_sel_hi:[1,0,1]
	v_lshl_add_u64 v[10:11], s[34:35], 0, v[94:95]
	v_lshl_add_u64 v[10:11], v[10:11], 0, v[92:93]
	s_addk_i32 s30, 0xb0
	global_store_dwordx4 v[10:11], v[14:17], off sc1
	v_pk_fma_f32 v[4:5], v[4:5], v[20:21], v[68:69] op_sel_hi:[1,0,1]
	v_pk_fma_f32 v[2:3], v[2:3], v[20:21], v[66:67] op_sel_hi:[1,0,1]
	s_ashr_i32 s31, s30, 31
	ds_write_b128 v114, v[6:9]
	ds_write_b128 v114, v[2:5] offset:16
	s_lshl_b64 s[30:31], s[30:31], 7
	ds_read_b128 v[2:5], v109
	ds_read_b128 v[6:9], v109 offset:1152
	s_add_u32 s30, s43, s30
	s_addc_u32 s31, s44, s31
	v_lshl_add_u64 v[10:11], s[30:31], 0, v[82:83]
	v_lshl_add_u64 v[10:11], v[10:11], 0, v[92:93]
	s_waitcnt lgkmcnt(1)
	global_store_dwordx4 v[10:11], v[2:5], off sc1
	s_nop 1
	v_lshl_add_u64 v[2:3], s[30:31], 0, v[94:95]
	v_lshl_add_u64 v[2:3], v[2:3], 0, v[92:93]
	s_waitcnt lgkmcnt(0)
	global_store_dwordx4 v[2:3], v[6:9], off sc1
	s_andn2_b64 vcc, exec, s[8:9]
	s_mov_b64 s[8:9], -1
	s_cbranch_vccnz .LBB0_2366

.LBB0_2896:
	s_or_b64 exec, exec, s[12:13]
	v_sub_f32_e32 v2, v47, v45
	v_mul_f32_e32 v2, 0x3fb8aa3b, v2
	v_exp_f32_e32 v4, v2
	v_sub_f32_e32 v2, v49, v45
	v_mul_f32_e32 v2, 0x3fb8aa3b, v2
	v_exp_f32_e32 v5, v2
	v_sub_f32_e32 v2, v50, v45
	v_mul_f32_e32 v2, 0x3fb8aa3b, v2
	v_exp_f32_e32 v3, v2
	v_add_f32_e32 v2, 1.0, v4
	v_add_f32_e32 v2, v2, v5
	v_add_f32_e32 v2, v2, v3
	v_div_scale_f32 v6, s[4:5], v2, v2, 1.0
	v_rcp_f32_e32 v7, v6
	s_nop 0
	v_fma_f32 v8, -v6, v7, 1.0
	v_fmac_f32_e32 v7, v8, v7
	v_div_scale_f32 v8, vcc, 1.0, v2, 1.0
	v_mul_f32_e32 v9, v8, v7
	v_fma_f32 v10, -v6, v9, v8
	v_fmac_f32_e32 v9, v10, v7
	v_fma_f32 v6, -v6, v9, v8
	v_div_fmas_f32 v6, v6, v7, v9
	v_div_fixup_f32 v2, v6, v2, 1.0
	v_lshlrev_b32_e32 v6, 16, v48
	v_lshlrev_b32_e32 v7, 24, v30
	v_lshl_or_b32 v6, v46, 8, v6
	v_or3_b32 v8, v6, v7, v44
	v_lshl_add_u64 v[6:7], v[38:39], 2, s[20:21]
	global_store_dword v[6:7], v8, off sc1
	v_pk_mul_f32 v[6:7], v[4:5], v[2:3] op_sel_hi:[1,0]
	v_mul_f32_e32 v5, v3, v2
	v_lshl_add_u64 v[8:9], v[38:39], 4, s[22:23]
	v_mov_b32_e32 v3, v6
	v_mov_b32_e32 v4, v7
	global_store_dwordx4 v[8:9], v[2:5], off sc1
	s_nop 1
	v_lshl_add_u32 v2, v44, 2, 0
	ds_add_u32 v2, v42
	v_lshl_add_u32 v2, v46, 2, 0
	ds_add_u32 v2, v42
	v_lshl_add_u32 v2, v48, 2, 0
	ds_add_u32 v2, v42
	v_lshl_add_u32 v2, v30, 2, 0
	ds_add_u32 v2, v42
.LBB0_2897:
	s_or_b64 exec, exec, s[28:29]
	s_waitcnt lgkmcnt(0)
	s_barrier
	s_and_saveexec_b64 s[12:13], s[8:9]
	s_cbranch_execz .LBB0_2384
	ds_read_b32 v4, v40
	v_lshl_add_u32 v2, s3, 5, v1
	v_ashrrev_i32_e32 v3, 31, v2
	v_lshl_add_u64 v[2:3], v[2:3], 2, s[24:25]
	s_waitcnt lgkmcnt(0)
	global_store_dword v[2:3], v4, off sc1
	s_branch .LBB0_2384

.LBB0_3203:
	v_ashrrev_i32_e32 v5, 31, v4
	v_lshlrev_b64 v[34:35], 2, v[4:5]
	v_lshl_add_u64 v[36:37], s[34:35], 0, v[34:35]
	global_store_dword v[36:37], v7, off sc1
	v_lshl_add_u64 v[6:7], s[38:39], 0, v[34:35]
	global_store_dword v[6:7], v22, off sc1
	v_lshl_add_u64 v[6:7], s[40:41], 0, v[34:35]
	v_mov_b32_e32 v9, v26
	v_mov_b32_e32 v11, v4
	v_lshl_add_u64 v[4:5], v[24:25], 2, s[30:31]
	global_store_dword v[6:7], v23, off sc1
	global_store_dwordx4 v[4:5], v[8:11], off sc1

.LBB0_3221:
	s_or_b64 exec, exec, s[20:21]
	s_cmp_eq_u32 s7, 0
	s_cselect_b64 s[20:21], -1, 0
	s_and_b64 s[22:23], s[20:21], s[14:15]
	s_and_saveexec_b64 s[20:21], s[22:23]
	s_cbranch_execz .LBB0_3223
	ds_read_b32 v1, v21 offset:2304
	s_waitcnt lgkmcnt(0)
	global_store_dword v[18:19], v1, off sc1

.LBB0_3241:
	s_waitcnt vmcnt(14)
	v_add_f32_e32 v1, v9, v11
	s_waitcnt vmcnt(12)
	v_add_f32_e32 v9, v23, v35
	v_add_f32_e32 v1, v1, v9
	s_waitcnt vmcnt(10)
	v_add_f32_e32 v9, v26, v36
	s_waitcnt vmcnt(8)
	v_add_f32_e32 v11, v37, v39
	v_add_f32_e32 v9, v9, v11
	v_add_f32_e32 v1, v1, v9
	s_waitcnt vmcnt(6)
	v_add_f32_e32 v9, v27, v38
	s_waitcnt vmcnt(4)
	v_add_f32_e32 v11, v40, v42
	v_add_f32_e32 v9, v9, v11
	s_waitcnt vmcnt(2)
	v_add_f32_e32 v11, v41, v43
	s_waitcnt vmcnt(0)
	v_add_f32_e32 v23, v44, v45
	v_add_f32_e32 v11, v11, v23
	v_add_f32_e32 v9, v9, v11
	v_add_f32_e32 v1, v1, v9
	v_ashrrev_i32_e32 v9, 31, v8
	v_lshlrev_b64 v[26:27], 2, v[8:9]
	v_lshl_add_u64 v[36:37], s[34:35], 0, v[26:27]
	global_store_dword v[36:37], v4, off sc1
	v_bfe_u32 v4, v33, 8, 8
	v_fmamk_f32 v1, v1, 0x3a800000, v31
	v_lshl_add_u32 v9, v4, 2, 0
	v_rsq_f32_e32 v23, v1
	ds_read_b32 v1, v9 offset:2560
	v_lshl_add_u64 v[36:37], s[38:39], 0, v[26:27]
	v_lshl_add_u64 v[26:27], s[40:41], 0, v[26:27]
	global_store_dword v[26:27], v23, off sc1
	s_and_b64 vcc, exec, s[22:23]
	s_waitcnt lgkmcnt(0)
	v_add_u32_e32 v26, v1, v10
	global_store_dword v[36:37], v22, off sc1
	s_cbranch_vccnz .LBB0_3253
	s_and_b64 vcc, exec, s[20:21]
	s_cbranch_vccnz .LBB0_3247
	s_andn2_b64 vcc, exec, s[48:49]
	s_cbranch_vccnz .LBB0_3248
	s_mov_b32 s73, 1
	v_mov_b32_e32 v1, 0
	s_mov_b32 s72, 0
	s_mov_b32 s33, s4

.LBB0_3253:
	v_ashrrev_i32_e32 v27, 31, v26
	v_lshlrev_b64 v[10:11], 2, v[26:27]
	v_bfe_u32 v1, v33, 16, 8
	v_lshl_add_u64 v[36:37], s[34:35], 0, v[10:11]
	v_lshl_add_u32 v4, v1, 2, 0
	global_store_dword v[36:37], v5, off sc1
	ds_read_b32 v5, v4 offset:2560
	v_lshl_add_u64 v[36:37], s[38:39], 0, v[10:11]
	v_lshl_add_u64 v[10:11], s[40:41], 0, v[10:11]
	global_store_dword v[10:11], v23, off sc1
	s_and_b64 vcc, exec, s[22:23]
	s_waitcnt lgkmcnt(0)
	v_add_u32_e32 v10, v5, v3
	global_store_dword v[36:37], v22, off sc1
	s_cbranch_vccnz .LBB0_3265
	s_and_b64 vcc, exec, s[20:21]
	s_cbranch_vccnz .LBB0_3259
	s_andn2_b64 vcc, exec, s[48:49]
	s_cbranch_vccnz .LBB0_3260
	s_mov_b32 s73, 1
	v_mov_b32_e32 v3, 0
	s_mov_b32 s72, 0
	s_mov_b32 s33, s4

.LBB0_3265:
	v_ashrrev_i32_e32 v11, 31, v10
	v_lshlrev_b64 v[36:37], 2, v[10:11]
	v_lshl_add_u64 v[4:5], s[34:35], 0, v[36:37]
	v_lshrrev_b32_e32 v3, 24, v33
	global_store_dword v[4:5], v6, off sc1
	v_lshl_add_u32 v5, v3, 2, 0
	ds_read_b32 v1, v5 offset:2560
	v_lshl_add_u64 v[38:39], s[38:39], 0, v[36:37]
	v_lshl_add_u64 v[36:37], s[40:41], 0, v[36:37]
	s_and_b64 vcc, exec, s[22:23]
	global_store_dword v[38:39], v22, off sc1
	s_waitcnt lgkmcnt(0)
	v_add_u32_e32 v4, v1, v34
	global_store_dword v[36:37], v23, off sc1
	s_cbranch_vccnz .LBB0_3203
	s_and_b64 vcc, exec, s[20:21]
	s_cbranch_vccnz .LBB0_3271
	s_andn2_b64 vcc, exec, s[48:49]
	s_cbranch_vccnz .LBB0_3272
	s_mov_b32 s21, 1
	v_mov_b32_e32 v1, 0
	s_mov_b32 s20, 0
	s_mov_b32 s22, s4

.LBB0_3485:
	s_or_b64 exec, exec, s[8:9]
	v_mov_b32_e32 v2, v0
	s_waitcnt lgkmcnt(0)
	s_barrier
	s_nop 0
	v_readfirstlane_b32 s0, v2
	s_ashr_i32 s1, s0, 6
	s_add_i32 s0, s1, s33
	s_cmp_lt_i32 s0, 0x10000
	s_cbranch_scc0 .LBB0_3488
	s_load_dwordx2 s[4:5], s[90:91], 0xc8
	v_and_b32_e32 v1, 63, v0
	v_lshlrev_b32_e32 v2, 4, v1
	v_lshlrev_b32_e32 v3, 3, v1
	v_mov_b32_e32 v5, 0
	v_mov_b32_e32 v6, 0x358637bd
	s_mov_b32 s16, 0x3e000000
	s_mov_b32 s17, 0
	s_waitcnt lgkmcnt(0)
	s_add_u32 s6, s4, 0xf00000
	s_addc_u32 s7, s5, 0
	s_add_u32 s8, s4, 0x1ec00000
	s_addc_u32 s9, s5, 0
	s_add_u32 s10, s4, 0x2ec00000
	s_addc_u32 s11, s5, 0
	s_add_u32 s14, s4, 0x5fc00000
	s_addc_u32 s15, s5, 0
	s_add_u32 s30, s4, 0x6bc00000
	s_addc_u32 s31, s5, 0
	s_add_i32 s1, s0, s54
	s_min_i32 s3, s0, 0xffff
	s_lshl_b32 s3, s3, 4
	s_add_u32 s34, s6, s3
	s_addc_u32 s35, s7, 0
	global_load_dwordx4 v[12:15], v5, s[34:35]
	s_min_i32 s3, s1, 0xffff
	s_lshl_b32 s3, s3, 4
	s_add_u32 s36, s6, s3
	s_addc_u32 s37, s7, 0
	global_load_dwordx4 v[16:19], v5, s[36:37]
	s_waitcnt vmcnt(1)
	v_readfirstlane_b32 s56, v12
	v_readfirstlane_b32 s57, v13
	v_readfirstlane_b32 s58, v14
	v_readfirstlane_b32 s59, v15
	s_min_i32 s3, s0, 0xffff
	s_lshl_b32 s3, s3, 11
	s_add_u32 s60, s8, s3
	s_addc_u32 s61, s9, 0
	global_load_dwordx4 v[20:23], v2, s[60:61]
	global_load_dwordx4 v[24:27], v2, s[60:61] offset:1024
	s_lshl_b32 s3, s56, 10
	s_add_u32 s68, s10, s3
	s_addc_u32 s69, s11, 0
	global_load_dwordx2 v[28:29], v3, s[68:69]
	global_load_dwordx2 v[36:37], v3, s[68:69] offset:512
	s_lshl_b32 s3, s57, 10
	s_add_u32 s72, s10, s3
	s_addc_u32 s73, s11, 0
	global_load_dwordx2 v[30:31], v3, s[72:73]
	global_load_dwordx2 v[38:39], v3, s[72:73] offset:512
	s_lshl_b32 s3, s58, 10
	s_add_u32 s74, s10, s3
	s_addc_u32 s75, s11, 0
	global_load_dwordx2 v[32:33], v3, s[74:75]
	global_load_dwordx2 v[40:41], v3, s[74:75] offset:512
	s_lshl_b32 s3, s59, 10
	s_add_u32 s78, s10, s3
	s_addc_u32 s79, s11, 0
	global_load_dwordx2 v[34:35], v3, s[78:79]
	global_load_dwordx2 v[42:43], v3, s[78:79] offset:512
	s_add_i32 s1, s0, s54
	s_add_i32 s13, s1, s54
	s_min_i32 s3, s13, 0xffff
	s_lshl_b32 s3, s3, 4
	s_add_u32 s34, s6, s3
	s_addc_u32 s35, s7, 0
	global_load_dwordx4 v[12:15], v5, s[34:35]
	s_waitcnt vmcnt(11)
	v_readfirstlane_b32 s56, v16
	v_readfirstlane_b32 s57, v17
	v_readfirstlane_b32 s58, v18
	v_readfirstlane_b32 s59, v19
	s_min_i32 s3, s1, 0xffff
	s_lshl_b32 s3, s3, 11
	s_add_u32 s60, s8, s3
	s_addc_u32 s61, s9, 0
	global_load_dwordx4 v[48:51], v2, s[60:61]
	global_load_dwordx4 v[52:55], v2, s[60:61] offset:1024
	s_lshl_b32 s3, s56, 10
	s_add_u32 s68, s10, s3
	s_addc_u32 s69, s11, 0
	global_load_dwordx2 v[56:57], v3, s[68:69]
	global_load_dwordx2 v[64:65], v3, s[68:69] offset:512
	s_lshl_b32 s3, s57, 10
	s_add_u32 s72, s10, s3
	s_addc_u32 s73, s11, 0
	global_load_dwordx2 v[58:59], v3, s[72:73]
	global_load_dwordx2 v[66:67], v3, s[72:73] offset:512
	s_lshl_b32 s3, s58, 10
	s_add_u32 s74, s10, s3
	s_addc_u32 s75, s11, 0
	global_load_dwordx2 v[60:61], v3, s[74:75]
	global_load_dwordx2 v[68:69], v3, s[74:75] offset:512
	s_lshl_b32 s3, s59, 10
	s_add_u32 s78, s10, s3
	s_addc_u32 s79, s11, 0
	global_load_dwordx2 v[62:63], v3, s[78:79]
	global_load_dwordx2 v[70:71], v3, s[78:79] offset:512
	s_waitcnt vmcnt(11)
	v_lshlrev_b32_e32 v80, 16, v20
	v_and_b32_e32 v81, 0xffff0000, v20
	v_lshlrev_b32_e32 v82, 16, v21
	v_and_b32_e32 v83, 0xffff0000, v21
	v_lshlrev_b32_e32 v84, 16, v22
	v_and_b32_e32 v85, 0xffff0000, v22
	v_lshlrev_b32_e32 v86, 16, v23
	v_and_b32_e32 v87, 0xffff0000, v23
	v_lshlrev_b32_e32 v88, 16, v24
	v_and_b32_e32 v89, 0xffff0000, v24
	v_lshlrev_b32_e32 v90, 16, v25
	v_and_b32_e32 v91, 0xffff0000, v25
	v_lshlrev_b32_e32 v92, 16, v26
	v_and_b32_e32 v93, 0xffff0000, v26
	v_lshlrev_b32_e32 v94, 16, v27
	v_and_b32_e32 v95, 0xffff0000, v27
	v_cvt_pk_f32_fp8_e32 v[96:97], v28
	v_cvt_pk_f32_fp8_sdwa v[98:99], v28 src0_sel:WORD_1
	v_cvt_pk_f32_fp8_e32 v[100:101], v29
	v_cvt_pk_f32_fp8_sdwa v[102:103], v29 src0_sel:WORD_1
	v_cvt_pk_f32_fp8_e32 v[104:105], v36
	v_cvt_pk_f32_fp8_sdwa v[106:107], v36 src0_sel:WORD_1
	v_cvt_pk_f32_fp8_e32 v[108:109], v37
	v_cvt_pk_f32_fp8_sdwa v[110:111], v37 src0_sel:WORD_1
	v_pk_fma_f32 v[80:81], v[96:97], s[16:17], v[80:81] op_sel_hi:[1,0,1]
	v_pk_fma_f32 v[82:83], v[98:99], s[16:17], v[82:83] op_sel_hi:[1,0,1]
	v_pk_fma_f32 v[84:85], v[100:101], s[16:17], v[84:85] op_sel_hi:[1,0,1]
	v_pk_fma_f32 v[86:87], v[102:103], s[16:17], v[86:87] op_sel_hi:[1,0,1]
	v_pk_fma_f32 v[88:89], v[104:105], s[16:17], v[88:89] op_sel_hi:[1,0,1]
	v_pk_fma_f32 v[90:91], v[106:107], s[16:17], v[90:91] op_sel_hi:[1,0,1]
	v_pk_fma_f32 v[92:93], v[108:109], s[16:17], v[92:93] op_sel_hi:[1,0,1]
	v_pk_fma_f32 v[94:95], v[110:111], s[16:17], v[94:95] op_sel_hi:[1,0,1]
	v_cvt_pk_f32_fp8_e32 v[96:97], v30
	v_cvt_pk_f32_fp8_sdwa v[98:99], v30 src0_sel:WORD_1
	v_cvt_pk_f32_fp8_e32 v[100:101], v31
	v_cvt_pk_f32_fp8_sdwa v[102:103], v31 src0_sel:WORD_1
	v_cvt_pk_f32_fp8_e32 v[104:105], v38
	v_cvt_pk_f32_fp8_sdwa v[106:107], v38 src0_sel:WORD_1
	v_cvt_pk_f32_fp8_e32 v[108:109], v39
	v_cvt_pk_f32_fp8_sdwa v[110:111], v39 src0_sel:WORD_1
	v_pk_fma_f32 v[80:81], v[96:97], s[16:17], v[80:81] op_sel_hi:[1,0,1]
	v_pk_fma_f32 v[82:83], v[98:99], s[16:17], v[82:83] op_sel_hi:[1,0,1]
	v_pk_fma_f32 v[84:85], v[100:101], s[16:17], v[84:85] op_sel_hi:[1,0,1]
	v_pk_fma_f32 v[86:87], v[102:103], s[16:17], v[86:87] op_sel_hi:[1,0,1]
	v_pk_fma_f32 v[88:89], v[104:105], s[16:17], v[88:89] op_sel_hi:[1,0,1]
	v_pk_fma_f32 v[90:91], v[106:107], s[16:17], v[90:91] op_sel_hi:[1,0,1]
	v_pk_fma_f32 v[92:93], v[108:109], s[16:17], v[92:93] op_sel_hi:[1,0,1]
	v_pk_fma_f32 v[94:95], v[110:111], s[16:17], v[94:95] op_sel_hi:[1,0,1]
	v_cvt_pk_f32_fp8_e32 v[96:97], v32
	v_cvt_pk_f32_fp8_sdwa v[98:99], v32 src0_sel:WORD_1
	v_cvt_pk_f32_fp8_e32 v[100:101], v33
	v_cvt_pk_f32_fp8_sdwa v[102:103], v33 src0_sel:WORD_1
	v_cvt_pk_f32_fp8_e32 v[104:105], v40
	v_cvt_pk_f32_fp8_sdwa v[106:107], v40 src0_sel:WORD_1
	v_cvt_pk_f32_fp8_e32 v[108:109], v41
	v_cvt_pk_f32_fp8_sdwa v[110:111], v41 src0_sel:WORD_1
	v_pk_fma_f32 v[80:81], v[96:97], s[16:17], v[80:81] op_sel_hi:[1,0,1]
	v_pk_fma_f32 v[82:83], v[98:99], s[16:17], v[82:83] op_sel_hi:[1,0,1]
	v_pk_fma_f32 v[84:85], v[100:101], s[16:17], v[84:85] op_sel_hi:[1,0,1]
	v_pk_fma_f32 v[86:87], v[102:103], s[16:17], v[86:87] op_sel_hi:[1,0,1]
	v_pk_fma_f32 v[88:89], v[104:105], s[16:17], v[88:89] op_sel_hi:[1,0,1]
	v_pk_fma_f32 v[90:91], v[106:107], s[16:17], v[90:91] op_sel_hi:[1,0,1]
	v_pk_fma_f32 v[92:93], v[108:109], s[16:17], v[92:93] op_sel_hi:[1,0,1]
	v_pk_fma_f32 v[94:95], v[110:111], s[16:17], v[94:95] op_sel_hi:[1,0,1]
	v_cvt_pk_f32_fp8_e32 v[96:97], v34
	v_cvt_pk_f32_fp8_sdwa v[98:99], v34 src0_sel:WORD_1
	v_cvt_pk_f32_fp8_e32 v[100:101], v35
	v_cvt_pk_f32_fp8_sdwa v[102:103], v35 src0_sel:WORD_1
	v_cvt_pk_f32_fp8_e32 v[104:105], v42
	v_cvt_pk_f32_fp8_sdwa v[106:107], v42 src0_sel:WORD_1
	v_cvt_pk_f32_fp8_e32 v[108:109], v43
	v_cvt_pk_f32_fp8_sdwa v[110:111], v43 src0_sel:WORD_1
	v_pk_fma_f32 v[80:81], v[96:97], s[16:17], v[80:81] op_sel_hi:[1,0,1]
	v_pk_fma_f32 v[82:83], v[98:99], s[16:17], v[82:83] op_sel_hi:[1,0,1]
	v_pk_fma_f32 v[84:85], v[100:101], s[16:17], v[84:85] op_sel_hi:[1,0,1]
	v_pk_fma_f32 v[86:87], v[102:103], s[16:17], v[86:87] op_sel_hi:[1,0,1]
	v_pk_fma_f32 v[88:89], v[104:105], s[16:17], v[88:89] op_sel_hi:[1,0,1]
	v_pk_fma_f32 v[90:91], v[106:107], s[16:17], v[90:91] op_sel_hi:[1,0,1]
	v_pk_fma_f32 v[92:93], v[108:109], s[16:17], v[92:93] op_sel_hi:[1,0,1]
	v_pk_fma_f32 v[94:95], v[110:111], s[16:17], v[94:95] op_sel_hi:[1,0,1]
	v_pk_mul_f32 v[116:117], v[80:81], v[80:81]
	v_pk_mul_f32 v[118:119], v[82:83], v[82:83]
	v_pk_mul_f32 v[120:121], v[84:85], v[84:85]
	v_pk_mul_f32 v[122:123], v[86:87], v[86:87]
	v_pk_mul_f32 v[124:125], v[88:89], v[88:89]
	v_pk_mul_f32 v[126:127], v[90:91], v[90:91]
	v_pk_mul_f32 v[128:129], v[92:93], v[92:93]
	v_pk_mul_f32 v[130:131], v[94:95], v[94:95]
	v_add_f32_e32 v112, v116, v117
	v_add_f32_e32 v112, v118, v112
	v_add_f32_e32 v112, v119, v112
	v_add_f32_e32 v112, v120, v112
	v_add_f32_e32 v112, v121, v112
	v_add_f32_e32 v112, v122, v112
	v_add_f32_e32 v112, v123, v112
	v_add_f32_e32 v112, v124, v112
	v_add_f32_e32 v112, v125, v112
	v_add_f32_e32 v112, v126, v112
	v_add_f32_e32 v112, v127, v112
	v_add_f32_e32 v112, v128, v112
	v_add_f32_e32 v112, v129, v112
	v_add_f32_e32 v112, v130, v112
	v_add_f32_e32 v112, v131, v112
	v_cvt_pk_bf16_f32 v132, v80, v81
	v_cvt_pk_bf16_f32 v133, v82, v83
	v_cvt_pk_bf16_f32 v134, v84, v85
	v_cvt_pk_bf16_f32 v135, v86, v87
	v_cvt_pk_bf16_f32 v136, v88, v89
	v_cvt_pk_bf16_f32 v137, v90, v91
	v_cvt_pk_bf16_f32 v138, v92, v93
	v_cvt_pk_bf16_f32 v139, v94, v95
	s_lshl_b32 s3, s0, 11
	s_add_u32 s62, s14, s3
	s_addc_u32 s65, s15, 0
	v_add_f32_dpp v112, v112, v112 quad_perm:[1,0,3,2] row_mask:0xf bank_mask:0xf
	s_mov_b32 s80, s62
	s_mov_b32 s81, s65
	v_add_f32_dpp v112, v112, v112 quad_perm:[2,3,0,1] row_mask:0xf bank_mask:0xf
	s_lshl_b32 s3, s0, 10
	s_add_u32 s82, s30, s3
	v_add_f32_dpp v112, v112, v112 row_half_mirror row_mask:0xf bank_mask:0xf
	s_addc_u32 s83, s31, 0
	s_nop 0
	v_add_f32_dpp v112, v112, v112 row_mirror row_mask:0xf bank_mask:0xf
	s_nop 1
	v_add_f32_dpp v112, v112, v112 row_bcast:15 row_mask:0xa bank_mask:0xf
	s_nop 1
	v_add_f32_dpp v112, v112, v112 row_bcast:31 row_mask:0xc bank_mask:0xf
	global_store_dwordx4 v2, v[132:135], s[80:81] sc1
	global_store_dwordx4 v2, v[136:139], s[80:81] offset:1024 sc1
	v_readlane_b32 s41, v112, 63
	s_nop 3
	v_mov_b32_e32 v114, s41
	v_fmamk_f32 v114, v114, 0x3a800000, v6
	v_rsq_f32_e32 v114, v114
	s_nop 0
	v_mul_f32_e32 v116, v80, v114
	v_mul_f32_e32 v117, v81, v114
	v_mul_f32_e32 v118, v82, v114
	v_mul_f32_e32 v119, v83, v114
	v_mul_f32_e32 v120, v84, v114
	v_mul_f32_e32 v121, v85, v114
	v_mul_f32_e32 v122, v86, v114
	v_mul_f32_e32 v123, v87, v114
	v_mul_f32_e32 v124, v88, v114
	v_mul_f32_e32 v125, v89, v114
	v_mul_f32_e32 v126, v90, v114
	v_mul_f32_e32 v127, v91, v114
	v_mul_f32_e32 v128, v92, v114
	v_mul_f32_e32 v129, v93, v114
	v_mul_f32_e32 v130, v94, v114
	v_mul_f32_e32 v131, v95, v114
	v_cvt_pk_fp8_f32 v140, v116, v117
	v_cvt_pk_fp8_f32 v141, v120, v121
	v_cvt_pk_fp8_f32 v142, v124, v125
	v_cvt_pk_fp8_f32 v143, v128, v129
	v_cvt_pk_fp8_f32 v140, v118, v119 op_sel:[0,0,1]
	v_cvt_pk_fp8_f32 v141, v122, v123 op_sel:[0,0,1]
	v_cvt_pk_fp8_f32 v142, v126, v127 op_sel:[0,0,1]
	v_cvt_pk_fp8_f32 v143, v130, v131 op_sel:[0,0,1]
	s_nop 0
	global_store_dwordx2 v3, v[140:141], s[82:83] sc1
	global_store_dwordx2 v3, v[142:143], s[82:83] offset:512 sc1
	s_mov_b32 s0, s1
	s_cmp_lt_i32 s0, 0x10000
	s_cbranch_scc0 .Lcmb1_done
.Lcmb1_loop:
	s_add_i32 s1, s0, s54
	s_add_i32 s13, s1, s54
	s_min_i32 s3, s13, 0xffff
	s_lshl_b32 s3, s3, 4
	s_add_u32 s36, s6, s3
	s_addc_u32 s37, s7, 0
	global_load_dwordx4 v[16:19], v5, s[36:37]
	s_waitcnt vmcnt(15)
	v_readfirstlane_b32 s56, v12
	v_readfirstlane_b32 s57, v13
	v_readfirstlane_b32 s58, v14
	v_readfirstlane_b32 s59, v15
	s_min_i32 s3, s1, 0xffff
	s_lshl_b32 s3, s3, 11
	s_add_u32 s60, s8, s3
	s_addc_u32 s61, s9, 0
	global_load_dwordx4 v[20:23], v2, s[60:61]
	global_load_dwordx4 v[24:27], v2, s[60:61] offset:1024
	s_lshl_b32 s3, s56, 10
	s_add_u32 s68, s10, s3
	s_addc_u32 s69, s11, 0
	global_load_dwordx2 v[28:29], v3, s[68:69]
	global_load_dwordx2 v[36:37], v3, s[68:69] offset:512
	s_lshl_b32 s3, s57, 10
	s_add_u32 s72, s10, s3
	s_addc_u32 s73, s11, 0
	global_load_dwordx2 v[30:31], v3, s[72:73]
	global_load_dwordx2 v[38:39], v3, s[72:73] offset:512
	s_lshl_b32 s3, s58, 10
	s_add_u32 s74, s10, s3
	s_addc_u32 s75, s11, 0
	global_load_dwordx2 v[32:33], v3, s[74:75]
	global_load_dwordx2 v[40:41], v3, s[74:75] offset:512
	s_lshl_b32 s3, s59, 10
	s_add_u32 s78, s10, s3
	s_addc_u32 s79, s11, 0
	global_load_dwordx2 v[34:35], v3, s[78:79]
	global_load_dwordx2 v[42:43], v3, s[78:79] offset:512
	s_waitcnt vmcnt(15)
	v_lshlrev_b32_e32 v80, 16, v48
	v_and_b32_e32 v81, 0xffff0000, v48
	v_lshlrev_b32_e32 v82, 16, v49
	v_and_b32_e32 v83, 0xffff0000, v49
	v_lshlrev_b32_e32 v84, 16, v50
	v_and_b32_e32 v85, 0xffff0000, v50
	v_lshlrev_b32_e32 v86, 16, v51
	v_and_b32_e32 v87, 0xffff0000, v51
	v_lshlrev_b32_e32 v88, 16, v52
	v_and_b32_e32 v89, 0xffff0000, v52
	v_lshlrev_b32_e32 v90, 16, v53
	v_and_b32_e32 v91, 0xffff0000, v53
	v_lshlrev_b32_e32 v92, 16, v54
	v_and_b32_e32 v93, 0xffff0000, v54
	v_lshlrev_b32_e32 v94, 16, v55
	v_and_b32_e32 v95, 0xffff0000, v55
	v_cvt_pk_f32_fp8_e32 v[96:97], v56
	v_cvt_pk_f32_fp8_sdwa v[98:99], v56 src0_sel:WORD_1
	v_cvt_pk_f32_fp8_e32 v[100:101], v57
	v_cvt_pk_f32_fp8_sdwa v[102:103], v57 src0_sel:WORD_1
	v_cvt_pk_f32_fp8_e32 v[104:105], v64
	v_cvt_pk_f32_fp8_sdwa v[106:107], v64 src0_sel:WORD_1
	v_cvt_pk_f32_fp8_e32 v[108:109], v65
	v_cvt_pk_f32_fp8_sdwa v[110:111], v65 src0_sel:WORD_1
	v_pk_fma_f32 v[80:81], v[96:97], s[16:17], v[80:81] op_sel_hi:[1,0,1]
	v_pk_fma_f32 v[82:83], v[98:99], s[16:17], v[82:83] op_sel_hi:[1,0,1]
	v_pk_fma_f32 v[84:85], v[100:101], s[16:17], v[84:85] op_sel_hi:[1,0,1]
	v_pk_fma_f32 v[86:87], v[102:103], s[16:17], v[86:87] op_sel_hi:[1,0,1]
	v_pk_fma_f32 v[88:89], v[104:105], s[16:17], v[88:89] op_sel_hi:[1,0,1]
	v_pk_fma_f32 v[90:91], v[106:107], s[16:17], v[90:91] op_sel_hi:[1,0,1]
	v_pk_fma_f32 v[92:93], v[108:109], s[16:17], v[92:93] op_sel_hi:[1,0,1]
	v_pk_fma_f32 v[94:95], v[110:111], s[16:17], v[94:95] op_sel_hi:[1,0,1]
	v_cvt_pk_f32_fp8_e32 v[96:97], v58
	v_cvt_pk_f32_fp8_sdwa v[98:99], v58 src0_sel:WORD_1
	v_cvt_pk_f32_fp8_e32 v[100:101], v59
	v_cvt_pk_f32_fp8_sdwa v[102:103], v59 src0_sel:WORD_1
	v_cvt_pk_f32_fp8_e32 v[104:105], v66
	v_cvt_pk_f32_fp8_sdwa v[106:107], v66 src0_sel:WORD_1
	v_cvt_pk_f32_fp8_e32 v[108:109], v67
	v_cvt_pk_f32_fp8_sdwa v[110:111], v67 src0_sel:WORD_1
	v_pk_fma_f32 v[80:81], v[96:97], s[16:17], v[80:81] op_sel_hi:[1,0,1]
	v_pk_fma_f32 v[82:83], v[98:99], s[16:17], v[82:83] op_sel_hi:[1,0,1]
	v_pk_fma_f32 v[84:85], v[100:101], s[16:17], v[84:85] op_sel_hi:[1,0,1]
	v_pk_fma_f32 v[86:87], v[102:103], s[16:17], v[86:87] op_sel_hi:[1,0,1]
	v_pk_fma_f32 v[88:89], v[104:105], s[16:17], v[88:89] op_sel_hi:[1,0,1]
	v_pk_fma_f32 v[90:91], v[106:107], s[16:17], v[90:91] op_sel_hi:[1,0,1]
	v_pk_fma_f32 v[92:93], v[108:109], s[16:17], v[92:93] op_sel_hi:[1,0,1]
	v_pk_fma_f32 v[94:95], v[110:111], s[16:17], v[94:95] op_sel_hi:[1,0,1]
	v_cvt_pk_f32_fp8_e32 v[96:97], v60
	v_cvt_pk_f32_fp8_sdwa v[98:99], v60 src0_sel:WORD_1
	v_cvt_pk_f32_fp8_e32 v[100:101], v61
	v_cvt_pk_f32_fp8_sdwa v[102:103], v61 src0_sel:WORD_1
	v_cvt_pk_f32_fp8_e32 v[104:105], v68
	v_cvt_pk_f32_fp8_sdwa v[106:107], v68 src0_sel:WORD_1
	v_cvt_pk_f32_fp8_e32 v[108:109], v69
	v_cvt_pk_f32_fp8_sdwa v[110:111], v69 src0_sel:WORD_1
	v_pk_fma_f32 v[80:81], v[96:97], s[16:17], v[80:81] op_sel_hi:[1,0,1]
	v_pk_fma_f32 v[82:83], v[98:99], s[16:17], v[82:83] op_sel_hi:[1,0,1]
	v_pk_fma_f32 v[84:85], v[100:101], s[16:17], v[84:85] op_sel_hi:[1,0,1]
	v_pk_fma_f32 v[86:87], v[102:103], s[16:17], v[86:87] op_sel_hi:[1,0,1]
	v_pk_fma_f32 v[88:89], v[104:105], s[16:17], v[88:89] op_sel_hi:[1,0,1]
	v_pk_fma_f32 v[90:91], v[106:107], s[16:17], v[90:91] op_sel_hi:[1,0,1]
	v_pk_fma_f32 v[92:93], v[108:109], s[16:17], v[92:93] op_sel_hi:[1,0,1]
	v_pk_fma_f32 v[94:95], v[110:111], s[16:17], v[94:95] op_sel_hi:[1,0,1]
	v_cvt_pk_f32_fp8_e32 v[96:97], v62
	v_cvt_pk_f32_fp8_sdwa v[98:99], v62 src0_sel:WORD_1
	v_cvt_pk_f32_fp8_e32 v[100:101], v63
	v_cvt_pk_f32_fp8_sdwa v[102:103], v63 src0_sel:WORD_1
	v_cvt_pk_f32_fp8_e32 v[104:105], v70
	v_cvt_pk_f32_fp8_sdwa v[106:107], v70 src0_sel:WORD_1
	v_cvt_pk_f32_fp8_e32 v[108:109], v71
	v_cvt_pk_f32_fp8_sdwa v[110:111], v71 src0_sel:WORD_1
	v_pk_fma_f32 v[80:81], v[96:97], s[16:17], v[80:81] op_sel_hi:[1,0,1]
	v_pk_fma_f32 v[82:83], v[98:99], s[16:17], v[82:83] op_sel_hi:[1,0,1]
	v_pk_fma_f32 v[84:85], v[100:101], s[16:17], v[84:85] op_sel_hi:[1,0,1]
	v_pk_fma_f32 v[86:87], v[102:103], s[16:17], v[86:87] op_sel_hi:[1,0,1]
	v_pk_fma_f32 v[88:89], v[104:105], s[16:17], v[88:89] op_sel_hi:[1,0,1]
	v_pk_fma_f32 v[90:91], v[106:107], s[16:17], v[90:91] op_sel_hi:[1,0,1]
	v_pk_fma_f32 v[92:93], v[108:109], s[16:17], v[92:93] op_sel_hi:[1,0,1]
	v_pk_fma_f32 v[94:95], v[110:111], s[16:17], v[94:95] op_sel_hi:[1,0,1]
	v_pk_mul_f32 v[116:117], v[80:81], v[80:81]
	v_pk_mul_f32 v[118:119], v[82:83], v[82:83]
	v_pk_mul_f32 v[120:121], v[84:85], v[84:85]
	v_pk_mul_f32 v[122:123], v[86:87], v[86:87]
	v_pk_mul_f32 v[124:125], v[88:89], v[88:89]
	v_pk_mul_f32 v[126:127], v[90:91], v[90:91]
	v_pk_mul_f32 v[128:129], v[92:93], v[92:93]
	v_pk_mul_f32 v[130:131], v[94:95], v[94:95]
	v_add_f32_e32 v112, v116, v117
	v_add_f32_e32 v112, v118, v112
	v_add_f32_e32 v112, v119, v112
	v_add_f32_e32 v112, v120, v112
	v_add_f32_e32 v112, v121, v112
	v_add_f32_e32 v112, v122, v112
	v_add_f32_e32 v112, v123, v112
	v_add_f32_e32 v112, v124, v112
	v_add_f32_e32 v112, v125, v112
	v_add_f32_e32 v112, v126, v112
	v_add_f32_e32 v112, v127, v112
	v_add_f32_e32 v112, v128, v112
	v_add_f32_e32 v112, v129, v112
	v_add_f32_e32 v112, v130, v112
	v_add_f32_e32 v112, v131, v112
	v_cvt_pk_bf16_f32 v132, v80, v81
	v_cvt_pk_bf16_f32 v133, v82, v83
	v_cvt_pk_bf16_f32 v134, v84, v85
	v_cvt_pk_bf16_f32 v135, v86, v87
	v_cvt_pk_bf16_f32 v136, v88, v89
	v_cvt_pk_bf16_f32 v137, v90, v91
	v_cvt_pk_bf16_f32 v138, v92, v93
	v_cvt_pk_bf16_f32 v139, v94, v95
	s_lshl_b32 s3, s0, 11
	s_add_u32 s62, s14, s3
	s_addc_u32 s65, s15, 0
	v_add_f32_dpp v112, v112, v112 quad_perm:[1,0,3,2] row_mask:0xf bank_mask:0xf
	s_mov_b32 s80, s62
	s_mov_b32 s81, s65
	v_add_f32_dpp v112, v112, v112 quad_perm:[2,3,0,1] row_mask:0xf bank_mask:0xf
	s_lshl_b32 s3, s0, 10
	s_add_u32 s82, s30, s3
	v_add_f32_dpp v112, v112, v112 row_half_mirror row_mask:0xf bank_mask:0xf
	s_addc_u32 s83, s31, 0
	s_nop 0
	v_add_f32_dpp v112, v112, v112 row_mirror row_mask:0xf bank_mask:0xf
	s_nop 1
	v_add_f32_dpp v112, v112, v112 row_bcast:15 row_mask:0xa bank_mask:0xf
	s_nop 1
	v_add_f32_dpp v112, v112, v112 row_bcast:31 row_mask:0xc bank_mask:0xf
	global_store_dwordx4 v2, v[132:135], s[80:81] sc1
	global_store_dwordx4 v2, v[136:139], s[80:81] offset:1024 sc1
	v_readlane_b32 s41, v112, 63
	s_nop 3
	v_mov_b32_e32 v114, s41
	v_fmamk_f32 v114, v114, 0x3a800000, v6
	v_rsq_f32_e32 v114, v114
	s_nop 0
	v_mul_f32_e32 v116, v80, v114
	v_mul_f32_e32 v117, v81, v114
	v_mul_f32_e32 v118, v82, v114
	v_mul_f32_e32 v119, v83, v114
	v_mul_f32_e32 v120, v84, v114
	v_mul_f32_e32 v121, v85, v114
	v_mul_f32_e32 v122, v86, v114
	v_mul_f32_e32 v123, v87, v114
	v_mul_f32_e32 v124, v88, v114
	v_mul_f32_e32 v125, v89, v114
	v_mul_f32_e32 v126, v90, v114
	v_mul_f32_e32 v127, v91, v114
	v_mul_f32_e32 v128, v92, v114
	v_mul_f32_e32 v129, v93, v114
	v_mul_f32_e32 v130, v94, v114
	v_mul_f32_e32 v131, v95, v114
	v_cvt_pk_fp8_f32 v140, v116, v117
	v_cvt_pk_fp8_f32 v141, v120, v121
	v_cvt_pk_fp8_f32 v142, v124, v125
	v_cvt_pk_fp8_f32 v143, v128, v129
	v_cvt_pk_fp8_f32 v140, v118, v119 op_sel:[0,0,1]
	v_cvt_pk_fp8_f32 v141, v122, v123 op_sel:[0,0,1]
	v_cvt_pk_fp8_f32 v142, v126, v127 op_sel:[0,0,1]
	v_cvt_pk_fp8_f32 v143, v130, v131 op_sel:[0,0,1]
	s_nop 0
	global_store_dwordx2 v3, v[140:141], s[82:83] sc1
	global_store_dwordx2 v3, v[142:143], s[82:83] offset:512 sc1
	s_mov_b32 s0, s1
	s_cmp_lt_i32 s0, 0x10000
	s_cbranch_scc0 .Lcmb1_done
	s_add_i32 s1, s0, s54
	s_add_i32 s13, s1, s54
	s_min_i32 s3, s13, 0xffff
	s_lshl_b32 s3, s3, 4
	s_add_u32 s34, s6, s3
	s_addc_u32 s35, s7, 0
	global_load_dwordx4 v[12:15], v5, s[34:35]
	s_waitcnt vmcnt(15)
	v_readfirstlane_b32 s56, v16
	v_readfirstlane_b32 s57, v17
	v_readfirstlane_b32 s58, v18
	v_readfirstlane_b32 s59, v19
	s_min_i32 s3, s1, 0xffff
	s_lshl_b32 s3, s3, 11
	s_add_u32 s60, s8, s3
	s_addc_u32 s61, s9, 0
	global_load_dwordx4 v[48:51], v2, s[60:61]
	global_load_dwordx4 v[52:55], v2, s[60:61] offset:1024
	s_lshl_b32 s3, s56, 10
	s_add_u32 s68, s10, s3
	s_addc_u32 s69, s11, 0
	global_load_dwordx2 v[56:57], v3, s[68:69]
	global_load_dwordx2 v[64:65], v3, s[68:69] offset:512
	s_lshl_b32 s3, s57, 10
	s_add_u32 s72, s10, s3
	s_addc_u32 s73, s11, 0
	global_load_dwordx2 v[58:59], v3, s[72:73]
	global_load_dwordx2 v[66:67], v3, s[72:73] offset:512
	s_lshl_b32 s3, s58, 10
	s_add_u32 s74, s10, s3
	s_addc_u32 s75, s11, 0
	global_load_dwordx2 v[60:61], v3, s[74:75]
	global_load_dwordx2 v[68:69], v3, s[74:75] offset:512
	s_lshl_b32 s3, s59, 10
	s_add_u32 s78, s10, s3
	s_addc_u32 s79, s11, 0
	global_load_dwordx2 v[62:63], v3, s[78:79]
	global_load_dwordx2 v[70:71], v3, s[78:79] offset:512
	s_waitcnt vmcnt(15)
	v_lshlrev_b32_e32 v80, 16, v20
	v_and_b32_e32 v81, 0xffff0000, v20
	v_lshlrev_b32_e32 v82, 16, v21
	v_and_b32_e32 v83, 0xffff0000, v21
	v_lshlrev_b32_e32 v84, 16, v22
	v_and_b32_e32 v85, 0xffff0000, v22
	v_lshlrev_b32_e32 v86, 16, v23
	v_and_b32_e32 v87, 0xffff0000, v23
	v_lshlrev_b32_e32 v88, 16, v24
	v_and_b32_e32 v89, 0xffff0000, v24
	v_lshlrev_b32_e32 v90, 16, v25
	v_and_b32_e32 v91, 0xffff0000, v25
	v_lshlrev_b32_e32 v92, 16, v26
	v_and_b32_e32 v93, 0xffff0000, v26
	v_lshlrev_b32_e32 v94, 16, v27
	v_and_b32_e32 v95, 0xffff0000, v27
	v_cvt_pk_f32_fp8_e32 v[96:97], v28
	v_cvt_pk_f32_fp8_sdwa v[98:99], v28 src0_sel:WORD_1
	v_cvt_pk_f32_fp8_e32 v[100:101], v29
	v_cvt_pk_f32_fp8_sdwa v[102:103], v29 src0_sel:WORD_1
	v_cvt_pk_f32_fp8_e32 v[104:105], v36
	v_cvt_pk_f32_fp8_sdwa v[106:107], v36 src0_sel:WORD_1
	v_cvt_pk_f32_fp8_e32 v[108:109], v37
	v_cvt_pk_f32_fp8_sdwa v[110:111], v37 src0_sel:WORD_1
	v_pk_fma_f32 v[80:81], v[96:97], s[16:17], v[80:81] op_sel_hi:[1,0,1]
	v_pk_fma_f32 v[82:83], v[98:99], s[16:17], v[82:83] op_sel_hi:[1,0,1]
	v_pk_fma_f32 v[84:85], v[100:101], s[16:17], v[84:85] op_sel_hi:[1,0,1]
	v_pk_fma_f32 v[86:87], v[102:103], s[16:17], v[86:87] op_sel_hi:[1,0,1]
	v_pk_fma_f32 v[88:89], v[104:105], s[16:17], v[88:89] op_sel_hi:[1,0,1]
	v_pk_fma_f32 v[90:91], v[106:107], s[16:17], v[90:91] op_sel_hi:[1,0,1]
	v_pk_fma_f32 v[92:93], v[108:109], s[16:17], v[92:93] op_sel_hi:[1,0,1]
	v_pk_fma_f32 v[94:95], v[110:111], s[16:17], v[94:95] op_sel_hi:[1,0,1]
	v_cvt_pk_f32_fp8_e32 v[96:97], v30
	v_cvt_pk_f32_fp8_sdwa v[98:99], v30 src0_sel:WORD_1
	v_cvt_pk_f32_fp8_e32 v[100:101], v31
	v_cvt_pk_f32_fp8_sdwa v[102:103], v31 src0_sel:WORD_1
	v_cvt_pk_f32_fp8_e32 v[104:105], v38
	v_cvt_pk_f32_fp8_sdwa v[106:107], v38 src0_sel:WORD_1
	v_cvt_pk_f32_fp8_e32 v[108:109], v39
	v_cvt_pk_f32_fp8_sdwa v[110:111], v39 src0_sel:WORD_1
	v_pk_fma_f32 v[80:81], v[96:97], s[16:17], v[80:81] op_sel_hi:[1,0,1]
	v_pk_fma_f32 v[82:83], v[98:99], s[16:17], v[82:83] op_sel_hi:[1,0,1]
	v_pk_fma_f32 v[84:85], v[100:101], s[16:17], v[84:85] op_sel_hi:[1,0,1]
	v_pk_fma_f32 v[86:87], v[102:103], s[16:17], v[86:87] op_sel_hi:[1,0,1]
	v_pk_fma_f32 v[88:89], v[104:105], s[16:17], v[88:89] op_sel_hi:[1,0,1]
	v_pk_fma_f32 v[90:91], v[106:107], s[16:17], v[90:91] op_sel_hi:[1,0,1]
	v_pk_fma_f32 v[92:93], v[108:109], s[16:17], v[92:93] op_sel_hi:[1,0,1]
	v_pk_fma_f32 v[94:95], v[110:111], s[16:17], v[94:95] op_sel_hi:[1,0,1]
	v_cvt_pk_f32_fp8_e32 v[96:97], v32
	v_cvt_pk_f32_fp8_sdwa v[98:99], v32 src0_sel:WORD_1
	v_cvt_pk_f32_fp8_e32 v[100:101], v33
	v_cvt_pk_f32_fp8_sdwa v[102:103], v33 src0_sel:WORD_1
	v_cvt_pk_f32_fp8_e32 v[104:105], v40
	v_cvt_pk_f32_fp8_sdwa v[106:107], v40 src0_sel:WORD_1
	v_cvt_pk_f32_fp8_e32 v[108:109], v41
	v_cvt_pk_f32_fp8_sdwa v[110:111], v41 src0_sel:WORD_1
	v_pk_fma_f32 v[80:81], v[96:97], s[16:17], v[80:81] op_sel_hi:[1,0,1]
	v_pk_fma_f32 v[82:83], v[98:99], s[16:17], v[82:83] op_sel_hi:[1,0,1]
	v_pk_fma_f32 v[84:85], v[100:101], s[16:17], v[84:85] op_sel_hi:[1,0,1]
	v_pk_fma_f32 v[86:87], v[102:103], s[16:17], v[86:87] op_sel_hi:[1,0,1]
	v_pk_fma_f32 v[88:89], v[104:105], s[16:17], v[88:89] op_sel_hi:[1,0,1]
	v_pk_fma_f32 v[90:91], v[106:107], s[16:17], v[90:91] op_sel_hi:[1,0,1]
	v_pk_fma_f32 v[92:93], v[108:109], s[16:17], v[92:93] op_sel_hi:[1,0,1]
	v_pk_fma_f32 v[94:95], v[110:111], s[16:17], v[94:95] op_sel_hi:[1,0,1]
	v_cvt_pk_f32_fp8_e32 v[96:97], v34
	v_cvt_pk_f32_fp8_sdwa v[98:99], v34 src0_sel:WORD_1
	v_cvt_pk_f32_fp8_e32 v[100:101], v35
	v_cvt_pk_f32_fp8_sdwa v[102:103], v35 src0_sel:WORD_1
	v_cvt_pk_f32_fp8_e32 v[104:105], v42
	v_cvt_pk_f32_fp8_sdwa v[106:107], v42 src0_sel:WORD_1
	v_cvt_pk_f32_fp8_e32 v[108:109], v43
	v_cvt_pk_f32_fp8_sdwa v[110:111], v43 src0_sel:WORD_1
	v_pk_fma_f32 v[80:81], v[96:97], s[16:17], v[80:81] op_sel_hi:[1,0,1]
	v_pk_fma_f32 v[82:83], v[98:99], s[16:17], v[82:83] op_sel_hi:[1,0,1]
	v_pk_fma_f32 v[84:85], v[100:101], s[16:17], v[84:85] op_sel_hi:[1,0,1]
	v_pk_fma_f32 v[86:87], v[102:103], s[16:17], v[86:87] op_sel_hi:[1,0,1]
	v_pk_fma_f32 v[88:89], v[104:105], s[16:17], v[88:89] op_sel_hi:[1,0,1]
	v_pk_fma_f32 v[90:91], v[106:107], s[16:17], v[90:91] op_sel_hi:[1,0,1]
	v_pk_fma_f32 v[92:93], v[108:109], s[16:17], v[92:93] op_sel_hi:[1,0,1]
	v_pk_fma_f32 v[94:95], v[110:111], s[16:17], v[94:95] op_sel_hi:[1,0,1]
	v_pk_mul_f32 v[116:117], v[80:81], v[80:81]
	v_pk_mul_f32 v[118:119], v[82:83], v[82:83]
	v_pk_mul_f32 v[120:121], v[84:85], v[84:85]
	v_pk_mul_f32 v[122:123], v[86:87], v[86:87]
	v_pk_mul_f32 v[124:125], v[88:89], v[88:89]
	v_pk_mul_f32 v[126:127], v[90:91], v[90:91]
	v_pk_mul_f32 v[128:129], v[92:93], v[92:93]
	v_pk_mul_f32 v[130:131], v[94:95], v[94:95]
	v_add_f32_e32 v112, v116, v117
	v_add_f32_e32 v112, v118, v112
	v_add_f32_e32 v112, v119, v112
	v_add_f32_e32 v112, v120, v112
	v_add_f32_e32 v112, v121, v112
	v_add_f32_e32 v112, v122, v112
	v_add_f32_e32 v112, v123, v112
	v_add_f32_e32 v112, v124, v112
	v_add_f32_e32 v112, v125, v112
	v_add_f32_e32 v112, v126, v112
	v_add_f32_e32 v112, v127, v112
	v_add_f32_e32 v112, v128, v112
	v_add_f32_e32 v112, v129, v112
	v_add_f32_e32 v112, v130, v112
	v_add_f32_e32 v112, v131, v112
	v_cvt_pk_bf16_f32 v132, v80, v81
	v_cvt_pk_bf16_f32 v133, v82, v83
	v_cvt_pk_bf16_f32 v134, v84, v85
	v_cvt_pk_bf16_f32 v135, v86, v87
	v_cvt_pk_bf16_f32 v136, v88, v89
	v_cvt_pk_bf16_f32 v137, v90, v91
	v_cvt_pk_bf16_f32 v138, v92, v93
	v_cvt_pk_bf16_f32 v139, v94, v95
	s_lshl_b32 s3, s0, 11
	s_add_u32 s62, s14, s3
	s_addc_u32 s65, s15, 0
	v_add_f32_dpp v112, v112, v112 quad_perm:[1,0,3,2] row_mask:0xf bank_mask:0xf
	s_mov_b32 s80, s62
	s_mov_b32 s81, s65
	v_add_f32_dpp v112, v112, v112 quad_perm:[2,3,0,1] row_mask:0xf bank_mask:0xf
	s_lshl_b32 s3, s0, 10
	s_add_u32 s82, s30, s3
	v_add_f32_dpp v112, v112, v112 row_half_mirror row_mask:0xf bank_mask:0xf
	s_addc_u32 s83, s31, 0
	s_nop 0
	v_add_f32_dpp v112, v112, v112 row_mirror row_mask:0xf bank_mask:0xf
	s_nop 1
	v_add_f32_dpp v112, v112, v112 row_bcast:15 row_mask:0xa bank_mask:0xf
	s_nop 1
	v_add_f32_dpp v112, v112, v112 row_bcast:31 row_mask:0xc bank_mask:0xf
	global_store_dwordx4 v2, v[132:135], s[80:81] sc1
	global_store_dwordx4 v2, v[136:139], s[80:81] offset:1024 sc1
	v_readlane_b32 s41, v112, 63
	s_nop 3
	v_mov_b32_e32 v114, s41
	v_fmamk_f32 v114, v114, 0x3a800000, v6
	v_rsq_f32_e32 v114, v114
	s_nop 0
	v_mul_f32_e32 v116, v80, v114
	v_mul_f32_e32 v117, v81, v114
	v_mul_f32_e32 v118, v82, v114
	v_mul_f32_e32 v119, v83, v114
	v_mul_f32_e32 v120, v84, v114
	v_mul_f32_e32 v121, v85, v114
	v_mul_f32_e32 v122, v86, v114
	v_mul_f32_e32 v123, v87, v114
	v_mul_f32_e32 v124, v88, v114
	v_mul_f32_e32 v125, v89, v114
	v_mul_f32_e32 v126, v90, v114
	v_mul_f32_e32 v127, v91, v114
	v_mul_f32_e32 v128, v92, v114
	v_mul_f32_e32 v129, v93, v114
	v_mul_f32_e32 v130, v94, v114
	v_mul_f32_e32 v131, v95, v114
	v_cvt_pk_fp8_f32 v140, v116, v117
	v_cvt_pk_fp8_f32 v141, v120, v121
	v_cvt_pk_fp8_f32 v142, v124, v125
	v_cvt_pk_fp8_f32 v143, v128, v129
	v_cvt_pk_fp8_f32 v140, v118, v119 op_sel:[0,0,1]
	v_cvt_pk_fp8_f32 v141, v122, v123 op_sel:[0,0,1]
	v_cvt_pk_fp8_f32 v142, v126, v127 op_sel:[0,0,1]
	v_cvt_pk_fp8_f32 v143, v130, v131 op_sel:[0,0,1]
	s_nop 0
	global_store_dwordx2 v3, v[140:141], s[82:83] sc1
	global_store_dwordx2 v3, v[142:143], s[82:83] offset:512 sc1
	s_mov_b32 s0, s1
	s_cmp_lt_i32 s0, 0x10000
	s_cbranch_scc0 .Lcmb1_done
	s_branch .Lcmb1_loop
